# plus: P2 prep steps with saddr-form loads, loop-invariant lane offsets and two counted waits per step (about 70 fewer instructions per step)
# speedup vs baseline: 1.0252x; 1.0026x over previous
; DI int opaque_tid() { int t = threadIdx.x; asm volatile("" : "+v"(t)); return t; }
; DI void p2_hgrn_roles(Frame& F, ArgsP A) {
;     ...
;     for (int item = F.vcu; item < 256; item += F.G) {
;         const int bh = item >> 1, vhalf = item & 1, b = bh >> 4, h = bh & 15;
;         const size_t rb = (size_t)b * SEQ * D;
;         unsigned CR[72];
;         f32x16 S0, S1;
; #pragma unroll
;         for (int i = 0; i < 72; ++i) CR[i] = 0u;
; #pragma unroll
;         for (int i = 0; i < 16; ++i) { S0[i] = 0.f; S1[i] = 0.f; }
;     ...
;         if (prep) {
;             const int pt = opaque_tid() & 255, k2 = pt & 63, tgp = pt >> 6, v64 = pt & 63;
;             const bf16_t* qp = (const bf16_t*)(A->ws + WS_QA) + rb + (size_t)(8 * tgp) * D + h * 128 + 2 * k2; const bf16_t* fp = (const bf16_t*)(A->ws + WS_LF) + rb + (size_t)(8 * tgp) * D + h * 128 + 2 * k2;
;             const bf16_t* ip = (const bf16_t*)(A->ws + WS_IA) + rb + (size_t)(8 * tgp) * D + h * 128 + vhalf * 64 + v64;
;             h_load8<0>(CR, qp, fp, ip, 0); h_load8<1>(CR, qp, fp, ip, 1); h_load8<2>(CR, qp, fp, ip, 2); h_totals8<0>(CR, lds, tgp, k2);
.LBB0_405:
	s_ashr_i32 s6, s95, 5
	s_ashr_i32 s7, s6, 31
	s_bfe_u32 s9, s95, 0x40001
	s_and_b32 s8, s95, 1
	s_lshl_b64 s[52:53], s[6:7], 22
	s_and_b64 vcc, exec, s[36:37]
	s_waitcnt vmcnt(2)
	v_mov_b32_e32 v180, v3
	v_mov_b32_e32 v169, v3
	v_mov_b32_e32 v165, v3
	v_mov_b32_e32 v153, v3
	v_mov_b32_e32 v148, v3
	v_mov_b32_e32 v146, v3
	v_mov_b32_e32 v127, v3
	v_mov_b32_e32 v125, v3
	v_mov_b32_e32 v175, v3
	v_mov_b32_e32 v172, v3
	v_mov_b32_e32 v167, v3
	v_mov_b32_e32 v155, v3
	v_mov_b32_e32 v157, v3
	v_mov_b32_e32 v140, v3
	v_mov_b32_e32 v131, v3
	v_mov_b32_e32 v129, v3
	s_waitcnt vmcnt(0)
	v_mov_b32_e32 v182, v3
	v_mov_b32_e32 v178, v3
	v_mov_b32_e32 v162, v3
	v_mov_b32_e32 v160, v3
	v_mov_b32_e32 v151, v3
	v_mov_b32_e32 v134, v3
	v_mov_b32_e32 v138, v3
	v_mov_b32_e32 v135, v3
	v_mov_b32_e32 v181, v3
	v_mov_b32_e32 v170, v3
	v_mov_b32_e32 v166, v3
	v_mov_b32_e32 v154, v3
	v_mov_b32_e32 v149, v3
	v_mov_b32_e32 v147, v3
	v_mov_b32_e32 v128, v3
	v_mov_b32_e32 v126, v3
	v_mov_b32_e32 v176, v3
	v_mov_b32_e32 v173, v3
	v_mov_b32_e32 v168, v3
	v_mov_b32_e32 v156, v3
	v_mov_b32_e32 v158, v3
	v_mov_b32_e32 v141, v3
	v_mov_b32_e32 v132, v3
	v_mov_b32_e32 v130, v3
	v_mov_b32_e32 v183, v3
	v_mov_b32_e32 v179, v3
	v_mov_b32_e32 v163, v3
	v_mov_b32_e32 v161, v3
	v_mov_b32_e32 v152, v3
	v_mov_b32_e32 v136, v3
	v_mov_b32_e32 v139, v3
	v_mov_b32_e32 v137, v3
	v_mov_b32_e32 v187, v3
	v_mov_b32_e32 v190, v3
	v_mov_b32_e32 v192, v3
	v_mov_b32_e32 v191, v3
	v_mov_b32_e32 v186, v3
	v_mov_b32_e32 v188, v3
	v_mov_b32_e32 v185, v3
	v_mov_b32_e32 v189, v3
	v_mov_b32_e32 v174, v3
	v_mov_b32_e32 v171, v3
	v_mov_b32_e32 v164, v3
	v_mov_b32_e32 v150, v3
	v_mov_b32_e32 v144, v3
	v_mov_b32_e32 v133, v3
	v_mov_b32_e32 v122, v3
	v_mov_b32_e32 v121, v3
	v_mov_b32_e32 v177, v3
	v_mov_b32_e32 v184, v3
	v_mov_b32_e32 v159, v3
	v_mov_b32_e32 v145, v3
	v_mov_b32_e32 v143, v3
	v_mov_b32_e32 v123, v3
	v_mov_b32_e32 v124, v3
	v_mov_b32_e32 v142, v3
	s_cbranch_vccnz .LBB0_407
	v_lshlrev_b32_e32 v200, 9, v0
	v_and_b32_e32 v200, 0x18000, v200
	v_and_b32_e32 v201, 63, v0
	v_lshl_or_b32 v208, v201, 1, v200
	v_lshl_or_b32 v200, v201, 2, v200
	v_cndmask_b32_e64 v201, 0, 1, s[44:45]
	v_lshl_add_u32 v208, v201, 7, v208
	v_add_u32_e32 v201, 0x1000, v200
	v_add_u32_e32 v202, 0x2000, v200
	v_add_u32_e32 v203, 0x3000, v200
	v_add_u32_e32 v204, 0x4000, v200
	v_add_u32_e32 v205, 0x5000, v200
	v_add_u32_e32 v206, 0x6000, v200
	v_add_u32_e32 v207, 0x7000, v200
	v_add_u32_e32 v209, 0x1000, v208
	v_add_u32_e32 v210, 0x2000, v208
	v_add_u32_e32 v211, 0x3000, v208
	v_add_u32_e32 v212, 0x4000, v208
	v_add_u32_e32 v213, 0x5000, v208
	v_add_u32_e32 v214, 0x6000, v208
	v_add_u32_e32 v215, 0x7000, v208
	v_mov_b32_e32 v2, v0
	s_load_dwordx2 s[4:5], s[40:41], 0x98
	s_lshl_b64 s[10:11], s[52:53], 1
	s_lshl_b32 s48, s9, 8
	v_bfe_u32 v77, v2, 6, 2
	v_and_b32_e32 v76, 63, v2
	s_waitcnt lgkmcnt(0)
	s_add_u32 s4, s4, s10
	v_lshlrev_b32_e32 v2, 15, v77
	s_addc_u32 s5, s5, s11
	v_lshl_add_u64 v[8:9], s[4:5], 0, v[2:3]
	v_lshlrev_b32_e32 v6, 2, v76
	v_mov_b32_e32 v7, v3
	v_lshl_add_u64 v[8:9], v[8:9], 0, s[48:49]
	s_lshl_b32 s48, s8, 7
	v_lshlrev_b32_e32 v4, 1, v76
	v_mov_b32_e32 v5, v3
	v_lshl_add_u64 v[12:13], v[8:9], 0, v[6:7]
	v_lshl_add_u64 v[6:7], v[8:9], 0, s[48:49]
	s_mov_b32 s4, 0xa201000
	v_lshl_add_u64 v[10:11], v[6:7], 0, v[4:5]
	v_add_co_u32_e32 v4, vcc, s4, v12
	s_mov_b32 s4, 0xe201000
	s_nop 0
	v_addc_co_u32_e32 v5, vcc, 0, v13, vcc
	v_add_co_u32_e32 v14, vcc, s4, v12
	s_mov_b32 s4, 0x12201000
	s_nop 0
	v_addc_co_u32_e32 v15, vcc, 0, v13, vcc
	v_add_co_u32_e32 v6, vcc, s4, v10
	s_mov_b32 s4, 0xa203000
	s_nop 0
	v_addc_co_u32_e32 v7, vcc, 0, v11, vcc
	v_add_co_u32_e32 v24, vcc, s4, v12
	s_mov_b32 s4, 0xe203000
	s_nop 0
	v_addc_co_u32_e32 v25, vcc, 0, v13, vcc
	v_add_co_u32_e32 v20, vcc, s4, v12
	s_mov_b32 s4, 0x12203000
	s_nop 0
	v_addc_co_u32_e32 v21, vcc, 0, v13, vcc
	v_add_co_u32_e32 v8, vcc, s4, v10
	s_mov_b32 s4, 0xa205000
	s_nop 0
	v_addc_co_u32_e32 v9, vcc, 0, v11, vcc
	v_add_co_u32_e32 v28, vcc, s4, v12
	s_mov_b32 s4, 0xe205000
	s_nop 0
	v_addc_co_u32_e32 v29, vcc, 0, v13, vcc
	v_add_co_u32_e32 v22, vcc, s4, v12
	s_mov_b32 s4, 0x12205000
	s_nop 0
	v_addc_co_u32_e32 v23, vcc, 0, v13, vcc
	v_add_co_u32_e32 v16, vcc, s4, v10
	s_mov_b32 s4, 0xa207000
	s_nop 0
	v_addc_co_u32_e32 v17, vcc, 0, v11, vcc
	v_add_co_u32_e32 v18, vcc, s4, v12
	s_mov_b32 s4, 0xe207000
	s_nop 0
	v_addc_co_u32_e32 v19, vcc, 0, v13, vcc
	v_add_co_u32_e32 v32, vcc, s4, v12
	s_mov_b32 s4, 0x12207000
	s_nop 0
	v_addc_co_u32_e32 v33, vcc, 0, v13, vcc
	v_add_co_u32_e32 v26, vcc, s4, v10
	s_mov_b32 s4, 0xa221000
	s_nop 0
	v_addc_co_u32_e32 v27, vcc, 0, v11, vcc
	v_add_co_u32_e32 v30, vcc, s4, v12
	s_mov_b32 s4, 0xe221000
	s_nop 0
	v_addc_co_u32_e32 v31, vcc, 0, v13, vcc
	v_add_co_u32_e32 v34, vcc, s4, v12
	s_mov_b32 s4, 0x12221000
	s_nop 0
	v_addc_co_u32_e32 v35, vcc, 0, v13, vcc
	v_add_co_u32_e32 v36, vcc, s4, v10
	s_mov_b32 s4, 0xa223000
	s_nop 0
	v_addc_co_u32_e32 v37, vcc, 0, v11, vcc
	v_add_co_u32_e32 v38, vcc, s4, v12
	s_mov_b32 s4, 0xe223000
	s_nop 0
	v_addc_co_u32_e32 v39, vcc, 0, v13, vcc
	v_add_co_u32_e32 v40, vcc, s4, v12
	s_mov_b32 s4, 0x12223000
	s_nop 0
	v_addc_co_u32_e32 v41, vcc, 0, v13, vcc
	v_add_co_u32_e32 v42, vcc, s4, v10
	s_mov_b32 s4, 0xa225000
	s_nop 0
	v_addc_co_u32_e32 v43, vcc, 0, v11, vcc
	v_add_co_u32_e32 v44, vcc, s4, v12
	s_mov_b32 s4, 0xe225000
	s_nop 0
	v_addc_co_u32_e32 v45, vcc, 0, v13, vcc
	v_add_co_u32_e32 v46, vcc, s4, v12
	s_mov_b32 s4, 0x12225000
	s_nop 0
	v_addc_co_u32_e32 v47, vcc, 0, v13, vcc
	v_add_co_u32_e32 v48, vcc, s4, v10
	s_mov_b32 s4, 0xa227000
	s_nop 0
	v_addc_co_u32_e32 v49, vcc, 0, v11, vcc
; #define LAS __attribute__((address_space(3)))
; template <int SET> DI void h_load8(unsigned (&CR)[72], const bf16_t* qp, const bf16_t* fp, const bf16_t* ip, int c) {
; #pragma unroll
;     for (int j = 0; j < 8; ++j) { const size_t ro = (size_t)(32 * c + j) * D; CR[24 * SET + j] = *(const unsigned*)(qp + ro); CR[24 * SET + 8 + j] = *(const unsigned*)(fp + ro); CR[24 * SET + 16 + j] = ip[ro]; }
; }
; template <int SET> DI void h_totals8(const unsigned (&CR)[72], LAS unsigned char* buf, int tgp, int k2) {
;     float lo = 0.f, hi = 0.f;
; #pragma unroll
;     for (int j = 0; j < 8; ++j) { lo += bflo(CR[24 * SET + 8 + j]); hi += bfhi(CR[24 * SET + 8 + j]); }
;     *(LAS f32x2_t*)(buf + H_TOT + (tgp * 128 + 2 * k2) * 4) = (f32x2_t){lo, hi};
; }
	v_add_co_u32_e32 v50, vcc, s4, v12
	s_mov_b32 s4, 0xe227000
	s_nop 0
	v_addc_co_u32_e32 v51, vcc, 0, v13, vcc
	v_add_co_u32_e32 v52, vcc, s4, v12
	s_mov_b32 s4, 0x12227000
	s_nop 0
	v_addc_co_u32_e32 v53, vcc, 0, v13, vcc
	v_add_co_u32_e32 v54, vcc, s4, v10
	s_mov_b32 s4, 0xa241000
	s_nop 0
	v_addc_co_u32_e32 v55, vcc, 0, v11, vcc
	v_add_co_u32_e32 v56, vcc, s4, v12
	s_mov_b32 s4, 0xe241000
	s_nop 0
	v_addc_co_u32_e32 v57, vcc, 0, v13, vcc
	v_add_co_u32_e32 v58, vcc, s4, v12
	s_mov_b32 s4, 0x12241000
	s_nop 0
	v_addc_co_u32_e32 v59, vcc, 0, v13, vcc
	v_add_co_u32_e32 v60, vcc, s4, v10
	s_mov_b32 s4, 0xa243000
	s_nop 0
	v_addc_co_u32_e32 v61, vcc, 0, v11, vcc
	v_add_co_u32_e32 v62, vcc, s4, v12
	global_load_dword v123, v[24:25], off offset:-4096
	global_load_dword v143, v[24:25], off
	global_load_dword v121, v[14:15], off offset:-4096
	global_load_ushort v185, v[6:7], off
	global_load_dword v122, v[14:15], off
	global_load_dword v124, v[4:5], off
	v_addc_co_u32_e32 v63, vcc, 0, v13, vcc
	v_add_co_u32_e32 v64, vcc, s74, v12
	global_load_dword v145, v[28:29], off offset:-4096
	global_load_dword v164, v[22:23], off
	global_load_dword v159, v[28:29], off
	global_load_dword v133, v[20:21], off offset:-4096
	global_load_ushort v186, v[8:9], off
	global_load_dword v144, v[20:21], off
	v_addc_co_u32_e32 v65, vcc, 0, v13, vcc
	v_add_co_u32_e32 v66, vcc, s75, v10
	global_load_dword v150, v[22:23], off offset:-4096
	s_nop 0
	v_addc_co_u32_e32 v67, vcc, 0, v11, vcc
	v_add_co_u32_e32 v68, vcc, s76, v12
	global_load_dword v171, v[32:33], off offset:-4096
	global_load_ushort v187, v[26:27], off
	global_load_dword v174, v[32:33], off
	global_load_dword v177, v[18:19], off
	v_addc_co_u32_e32 v69, vcc, 0, v13, vcc
	v_add_co_u32_e32 v70, vcc, s77, v12
	v_lshlrev_b32_e32 v2, 9, v77
	s_nop 0
	v_addc_co_u32_e32 v71, vcc, 0, v13, vcc
	v_add_co_u32_e32 v72, vcc, s79, v12
	s_waitcnt vmcnt(14)
	v_lshlrev_b32_e32 v14, 16, v121
	v_addc_co_u32_e32 v73, vcc, 0, v13, vcc
	v_add_co_u32_e32 v12, vcc, s80, v12
	v_and_b32_e32 v15, 0xffff0000, v121
	s_nop 0
	v_addc_co_u32_e32 v13, vcc, 0, v13, vcc
	v_add_co_u32_e32 v74, vcc, s78, v10
	v_pk_add_f32 v[14:15], v[14:15], 0 op_sel_hi:[1,0]
	s_nop 0
	v_addc_co_u32_e32 v75, vcc, 0, v11, vcc
	v_add_co_u32_e32 v10, vcc, s81, v10
	s_waitcnt vmcnt(12)
	v_lshlrev_b32_e32 v24, 16, v122
	v_addc_co_u32_e32 v11, vcc, 0, v11, vcc
	global_load_ushort v188, v[8:9], off offset:-4096
	global_load_ushort v189, v[6:7], off offset:-4096
	global_load_dword v142, v[4:5], off offset:-4096
	global_load_ushort v190, v[26:27], off offset:-4096
	global_load_ushort v191, v[16:17], off offset:-4096
	global_load_ushort v192, v[16:17], off
	global_load_dword v184, v[18:19], off offset:-4096
	global_load_ushort v126, v[36:37], off offset:-4096
	global_load_ushort v128, v[36:37], off
	global_load_dword v136, v[38:39], off offset:-4096
	global_load_dword v152, v[38:39], off
	global_load_dword v130, v[34:35], off offset:-4096
	global_load_dword v132, v[34:35], off
	global_load_dword v137, v[30:31], off offset:-4096
	global_load_dword v139, v[30:31], off
	global_load_ushort v147, v[42:43], off offset:-4096
	global_load_ushort v149, v[42:43], off
	global_load_dword v156, v[46:47], off offset:-4096
	global_load_dword v168, v[46:47], off
	global_load_dword v161, v[44:45], off offset:-4096
	global_load_dword v163, v[44:45], off
	global_load_dword v141, v[40:41], off offset:-4096
	global_load_dword v158, v[40:41], off
	global_load_ushort v154, v[48:49], off offset:-4096
	global_load_ushort v166, v[48:49], off
	global_load_ushort v170, v[54:55], off offset:-4096
	global_load_ushort v181, v[54:55], off
	global_load_dword v173, v[52:53], off offset:-4096
	global_load_dword v176, v[52:53], off
	global_load_dword v179, v[50:51], off offset:-4096
	global_load_dword v183, v[50:51], off
	global_load_ushort v125, v[60:61], off offset:-4096
	global_load_ushort v127, v[60:61], off
	global_load_dword v134, v[62:63], off offset:-4096
	global_load_dword v151, v[62:63], off
	global_load_dword v129, v[58:59], off offset:-4096
	global_load_dword v131, v[58:59], off
	global_load_dword v135, v[56:57], off offset:-4096
	global_load_dword v138, v[56:57], off
	global_load_ushort v146, v[66:67], off offset:-4096
	global_load_ushort v148, v[66:67], off
	global_load_dword v155, v[70:71], off offset:-4096
	global_load_dword v167, v[70:71], off
	global_load_dword v160, v[68:69], off offset:-4096
	global_load_dword v162, v[68:69], off
	global_load_dword v140, v[64:65], off offset:-4096
	global_load_dword v157, v[64:65], off
	global_load_ushort v153, v[74:75], off offset:-4096
	global_load_ushort v165, v[74:75], off
	global_load_ushort v169, v[10:11], off offset:-4096
	global_load_ushort v180, v[10:11], off
	global_load_dword v172, v[12:13], off offset:-4096
	global_load_dword v175, v[12:13], off
	global_load_dword v178, v[72:73], off offset:-4096
	global_load_dword v182, v[72:73], off
	v_and_b32_e32 v25, 0xffff0000, v122
	v_pk_add_f32 v[14:15], v[14:15], v[24:25]
	s_waitcnt vmcnt(62)
	v_lshlrev_b32_e32 v20, 16, v133
	v_and_b32_e32 v21, 0xffff0000, v133
	v_pk_add_f32 v[14:15], v[14:15], v[20:21]
	s_waitcnt vmcnt(60)
	v_lshlrev_b32_e32 v20, 16, v144
	v_and_b32_e32 v21, 0xffff0000, v144
	v_pk_add_f32 v[14:15], v[14:15], v[20:21]
	s_waitcnt vmcnt(59)
	v_lshlrev_b32_e32 v20, 16, v150
	v_and_b32_e32 v21, 0xffff0000, v150
	v_pk_add_f32 v[14:15], v[14:15], v[20:21]
	v_lshlrev_b32_e32 v20, 16, v164
	v_and_b32_e32 v21, 0xffff0000, v164
	v_pk_add_f32 v[14:15], v[14:15], v[20:21]
	s_waitcnt vmcnt(58)
	v_lshlrev_b32_e32 v20, 16, v171
	v_and_b32_e32 v21, 0xffff0000, v171
	v_pk_add_f32 v[14:15], v[14:15], v[20:21]
	s_waitcnt vmcnt(56)
	v_lshlrev_b32_e32 v20, 16, v174
	v_and_b32_e32 v21, 0xffff0000, v174
	v_lshlrev_b32_e32 v4, 3, v76
	v_pk_add_f32 v[14:15], v[14:15], v[20:21]
	v_add3_u32 v2, 0, v2, v4
	ds_write_b64 v2, v[14:15] offset:41984

; DI int opaque_tid() { int t = threadIdx.x; asm volatile("" : "+v"(t)); return t; }
; DI void p2_hgrn_roles(Frame& F, ArgsP A) {
;     ...
;         const int bh = item >> 1, vhalf = item & 1, b = bh >> 4, h = bh & 15;
;         const size_t rb = (size_t)b * SEQ * D;
;         unsigned CR[72];
;         f32x16 S0, S1;
; #pragma unroll
;         for (int i = 0; i < 72; ++i) CR[i] = 0u;
; #pragma unroll
;         for (int i = 0; i < 16; ++i) { S0[i] = 0.f; S1[i] = 0.f; }
;     ...
;         if (prep) {
;             const int pt = opaque_tid() & 255, k2 = pt & 63, tgp = pt >> 6, v64 = pt & 63;
;             const bf16_t* qp = (const bf16_t*)(A->ws + WS_QA) + rb + (size_t)(8 * tgp) * D + h * 128 + 2 * k2; const bf16_t* fp = (const bf16_t*)(A->ws + WS_LF) + rb + (size_t)(8 * tgp) * D + h * 128 + 2 * k2;
;             const bf16_t* ip = (const bf16_t*)(A->ws + WS_IA) + rb + (size_t)(8 * tgp) * D + h * 128 + vhalf * 64 + v64;
;             h_load8<0>(CR, qp, fp, ip, 0); h_load8<1>(CR, qp, fp, ip, 1); h_load8<2>(CR, qp, fp, ip, 2); h_totals8<0>(CR, lds, tgp, k2);
;         }
;         __syncthreads();
;         if (prep) { const int pt = opaque_tid() & 255; h_prep8<0>(CR, lds, pt >> 6, pt & 63, pt & 63); h_totals8<1>(CR, lds + H_BUF, pt >> 6, pt & 63); }
;         __syncthreads();
.LBB0_411:
	s_lshr_b32 s4, s95, 1
	s_and_b32 s4, s4, 15
	s_lshl_b32 s4, s4, 8
	v_cndmask_b32_e64 v2, 0, 1, s[44:45]
	s_lshl_b64 s[54:55], s[6:7], 23
	v_lshlrev_b32_e32 v2, 7, v2
	s_or_b32 s54, s54, s4
	v_mov_b32_e32 v16, v3
	v_mov_b32_e32 v17, v3
	v_or_b32_e32 v116, s54, v2
	v_mov_b32_e32 v2, v3
	v_mov_b32_e32 v4, v3
	v_mov_b32_e32 v5, v3
	v_mov_b32_e32 v6, v3
	v_mov_b32_e32 v7, v3
	v_mov_b32_e32 v8, v3
	v_mov_b32_e32 v9, v3
	v_mov_b32_e32 v10, v3
	v_mov_b32_e32 v11, v3
	v_mov_b32_e32 v12, v3
	v_mov_b32_e32 v13, v3
	v_mov_b32_e32 v14, v3
	v_mov_b32_e32 v15, v3
	v_mov_b64_e32 v[50:51], v[16:17]
	v_mov_b64_e32 v[66:67], v[16:17]
	s_lshl_b32 s96, s9, 7
	s_lshl_b32 s48, s8, 6
	v_mov_b32_e32 v117, s55
	s_mov_b32 s39, 0
	s_mov_b64 s[56:57], 0
	s_mov_b32 s97, 0xffff0000
	s_movk_i32 s38, 0xc000
	v_mov_b64_e32 v[48:49], v[14:15]
	v_mov_b64_e32 v[46:47], v[12:13]
	v_mov_b64_e32 v[44:45], v[10:11]
	v_mov_b64_e32 v[42:43], v[8:9]
	v_mov_b64_e32 v[40:41], v[6:7]
	v_mov_b64_e32 v[38:39], v[4:5]
	v_mov_b64_e32 v[36:37], v[2:3]
	v_mov_b64_e32 v[64:65], v[14:15]
	v_mov_b64_e32 v[62:63], v[12:13]
	v_mov_b64_e32 v[60:61], v[10:11]
	v_mov_b64_e32 v[58:59], v[8:9]
	v_mov_b64_e32 v[56:57], v[6:7]
	v_mov_b64_e32 v[54:55], v[4:5]
	v_mov_b64_e32 v[52:53], v[2:3]
	s_waitcnt vmcnt(0)
	s_waitcnt lgkmcnt(0)
	s_barrier
	s_mov_b64 s[4:5], -1
	s_and_b64 vcc, exec, s[42:43]
	s_cbranch_vccz .LBB0_414
	s_branch .LBB0_413

; template <int SET> DI void h_load8(unsigned (&CR)[72], const bf16_t* qp, const bf16_t* fp, const bf16_t* ip, int c) {
; #pragma unroll
;     for (int j = 0; j < 8; ++j) { const size_t ro = (size_t)(32 * c + j) * D; CR[24 * SET + j] = *(const unsigned*)(qp + ro); CR[24 * SET + 8 + j] = *(const unsigned*)(fp + ro); CR[24 * SET + 16 + j] = ip[ro]; }
; }
; template <int SET> DI void h_totals8(const unsigned (&CR)[72], LAS unsigned char* buf, int tgp, int k2) {
;     float lo = 0.f, hi = 0.f;
; #pragma unroll
;     for (int j = 0; j < 8; ++j) { lo += bflo(CR[24 * SET + 8 + j]); hi += bfhi(CR[24 * SET + 8 + j]); }
;     *(LAS f32x2_t*)(buf + H_TOT + (tgp * 128 + 2 * k2) * 4) = (f32x2_t){lo, hi};
; }
; template <int SET> DI void h_prep8(const unsigned (&CR)[72], LAS unsigned char* buf, int tgp, int k2, int v64) {
; DI void h_reduce_store2(LAS unsigned char* red, bf16_t* op, int c, int pt) {
; #pragma unroll
;     for (int s2 = 0; s2 < 2; ++s2) {
;         const int s = pt + 256 * s2, t = s >> 4, c4 = s & 15;
;         const f32x4 a = *(const LAS f32x4*)(red + ((0 * 32 + t) * 64 + 4 * c4) * 4), b2 = *(const LAS f32x4*)(red + ((1 * 32 + t) * 64 + 4 * c4) * 4);
;         const f32x4 sm = a + b2;
;         u32x2 w; w.x = pk2(sm[0], sm[1]); w.y = pk2(sm[2], sm[3]);
;         *(u32x2*)(op + (size_t)(32 * c + t) * D + 4 * c4) = w;
;     }
; }
; template <int RF, int RN, int RNN> DI void h_prep_step(unsigned (&CR)[72], ArgsP A, LAS unsigned char* lds, int cc, size_t rb, int h, int vhalf) {
;     const int pt = opaque_tid() & 255, k2 = pt & 63, tgp = pt >> 6, v64 = pt & 63;
;     const bf16_t* QA = (const bf16_t*)(A->ws + WS_QA); const bf16_t* LF = (const bf16_t*)(A->ws + WS_LF); const bf16_t* IA = (const bf16_t*)(A->ws + WS_IA); bf16_t* OH = (bf16_t*)(A->ws + WS_OH);
;     if (cc + 3 < 64) {
;         const bf16_t* qp = QA + rb + (size_t)(8 * tgp) * D + h * 128 + 2 * k2; const bf16_t* fp = LF + rb + (size_t)(8 * tgp) * D + h * 128 + 2 * k2;
;         const bf16_t* ip = IA + rb + (size_t)(8 * tgp) * D + h * 128 + vhalf * 64 + v64;
;         h_load8<RF>(CR, qp, fp, ip, cc + 3);
;     }
;     if (cc >= 1) h_reduce_store2(lds + H_RED2 + ((cc - 1) & 1) * 16384, OH + rb + h * 128 + vhalf * 64, cc - 1, pt);
;     if (cc + 1 < 64) h_prep8<RN>(CR, lds + ((cc + 1) & 1) * H_BUF, tgp, k2, v64);
;     if (cc + 2 < 64) h_totals8<RNN>(CR, lds + ((cc + 2) & 1) * H_BUF, tgp, k2);
; }
.LBB0_414:
	s_andn2_b64 vcc, exec, s[4:5]
	s_cbranch_vccnz .LBB0_420
	v_mov_b32_e32 v4, v0
	s_load_dwordx2 s[4:5], s[40:41], 0x98
	s_waitcnt lgkmcnt(0)
	s_add_u32 s98, s4, s54
	s_addc_u32 s99, s5, s55
	s_add_u32 s98, s98, s56
	s_addc_u32 s99, s99, s57
	s_add_u32 s98, s98, 0xa260000
	s_addc_u32 s99, s99, 0
	v_lshlrev_b32_e32 v2, 9, v4
	v_and_b32_e32 v6, 63, v4
	v_and_b32_e32 v5, 0x18000, v2
	v_lshl_or_b32 v2, v6, 2, v5
	v_lshl_or_b32 v2, v6, 1, v5
	global_load_dword v142, v200, s[98:99]
	global_load_dword v124, v201, s[98:99]
	global_load_dword v123, v202, s[98:99]
	global_load_dword v143, v203, s[98:99]
	global_load_dword v145, v204, s[98:99]
	global_load_dword v159, v205, s[98:99]
	global_load_dword v184, v206, s[98:99]
	global_load_dword v177, v207, s[98:99]
	s_add_u32 s98, s98, 0x4000000
	s_addc_u32 s99, s99, 0
	global_load_dword v121, v200, s[98:99]
	global_load_dword v122, v201, s[98:99]
	global_load_dword v133, v202, s[98:99]
	global_load_dword v144, v203, s[98:99]
	global_load_dword v150, v204, s[98:99]
	global_load_dword v164, v205, s[98:99]
	global_load_dword v171, v206, s[98:99]
	global_load_dword v174, v207, s[98:99]
	s_add_u32 s98, s98, 0x4000000
	s_addc_u32 s99, s99, 0
	global_load_ushort v189, v208, s[98:99]
	global_load_ushort v185, v209, s[98:99]
	global_load_ushort v188, v210, s[98:99]
	global_load_ushort v186, v211, s[98:99]
	global_load_ushort v191, v212, s[98:99]
	global_load_ushort v192, v213, s[98:99]
	global_load_ushort v190, v214, s[98:99]
	global_load_ushort v187, v215, s[98:99]
	s_cmp_eq_u32 s56, 0
	s_cbranch_scc1 .LBB0_417
	s_and_b32 s6, s38, 0x4000
	s_add_i32 s6, s6, 0
	s_add_i32 s8, s6, 0x16800
	s_lshl_b64 s[6:7], s[52:53], 1
	s_add_u32 s4, s4, s6
	s_addc_u32 s5, s5, s7
	s_lshl_b32 s6, s96, 1
	v_lshlrev_b32_sdwa v2, v1, v4 dst_sel:DWORD dst_unused:UNUSED_PAD src0_sel:DWORD src1_sel:BYTE_0
	s_add_u32 s4, s4, s6
	v_and_b32_e32 v2, 60, v2
	v_lshrrev_b32_sdwa v15, v118, v4 dst_sel:DWORD dst_unused:UNUSED_PAD src0_sel:DWORD src1_sel:BYTE_0
	s_addc_u32 s5, s5, 0
	s_lshl_b32 s6, s48, 1
	v_lshlrev_b32_e32 v5, 2, v2
	v_lshlrev_b32_e32 v16, 8, v15
	s_add_u32 s4, s4, s6
	v_add3_u32 v5, s8, v5, v16
	s_addc_u32 s5, s5, 0
	v_lshlrev_b32_e32 v2, 1, v2
	ds_read_b128 v[16:19], v5
	ds_read_b128 v[20:23], v5 offset:8192
	v_lshl_add_u64 v[24:25], s[4:5], 0, v[2:3]
	v_lshl_add_u64 v[32:33], v[24:25], 0, s[50:51]
	ds_read_b128 v[24:27], v5 offset:4096
	ds_read_b128 v[28:31], v5 offset:12288
	v_lshl_add_u32 v2, v15, 11, s97
	s_waitcnt lgkmcnt(2)
	v_pk_add_f32 v[18:19], v[18:19], v[22:23]
	v_pk_add_f32 v[16:17], v[16:17], v[20:21]
	s_nop 0
	v_cvt_pk_bf16_f32 v16, v16, v17
	v_cvt_pk_bf16_f32 v17, v18, v19
	v_lshl_add_u64 v[18:19], v[2:3], 1, v[32:33]
	global_store_dwordx2 v[18:19], v[16:17], off
	s_waitcnt lgkmcnt(0)
	v_pk_add_f32 v[16:17], v[26:27], v[30:31]
	v_pk_add_f32 v[18:19], v[24:25], v[28:29]
	v_add_u32_e32 v2, 0x8000, v2
	v_cvt_pk_bf16_f32 v18, v18, v19
	v_cvt_pk_bf16_f32 v19, v16, v17
	v_lshl_add_u64 v[16:17], v[2:3], 1, v[32:33]
	global_store_dwordx2 v[16:17], v[18:19], off
.LBB0_417:
	s_andn2_b32 s4, 1, s39
	s_mul_i32 s4, s4, 0xb400
	s_add_i32 s8, s4, 0
	v_lshlrev_b32_e32 v15, 3, v6
	v_add_u32_e32 v17, s8, v15
	ds_read2st64_b64 v[18:21], v17 offset0:82 offset1:83
	ds_read2st64_b64 v[22:25], v17 offset0:84 offset1:85
	v_cmp_lt_u32_sdwa s[4:5], v4, v120 src0_sel:BYTE_0 src1_sel:DWORD
	v_cmp_gt_u32_sdwa vcc, v4, s88 src0_sel:BYTE_0 src1_sel:DWORD
	v_lshrrev_b32_sdwa v16, v119, v4 dst_sel:DWORD dst_unused:UNUSED_PAD src0_sel:DWORD src1_sel:BYTE_0
	s_waitcnt lgkmcnt(1)
	v_add_f32_e32 v2, 0, v18
	v_add_f32_e32 v5, 0, v19
	v_cndmask_b32_e64 v19, v2, 0, s[4:5]
	v_cndmask_b32_e64 v18, v5, 0, s[4:5]
	v_add_f32_e32 v26, v20, v19
	v_add_f32_e32 v27, v21, v18
	v_cndmask_b32_e32 v19, v19, v26, vcc
	v_cndmask_b32_e32 v4, v18, v27, vcc
	v_add_f32_e32 v18, v2, v20
	s_waitcnt lgkmcnt(0)
	v_add_f32_e32 v2, v22, v19
	v_cmp_eq_u32_e32 vcc, 3, v16
	v_add_f32_e32 v5, v5, v21
	v_add_f32_e32 v20, v23, v4
	v_cndmask_b32_e32 v19, v19, v2, vcc
	v_add_f32_e32 v2, v18, v22
	v_add_f32_e32 v2, v2, v24
	v_cndmask_b32_e32 v21, v4, v20, vcc
	v_add_f32_e32 v4, v5, v23
	v_sub_f32_e32 v2, v2, v18
	v_sub_f32_e32 v19, v19, v18
	v_add_f32_e32 v20, v4, v25
	v_mul_f32_e32 v2, 0x3fb8aa3b, v2
	v_mul_f32_e32 v19, 0x3fb8aa3b, v19
	v_exp_f32_e32 v4, v2
	v_sub_f32_e32 v2, v20, v5
	v_exp_f32_e32 v20, v19
	v_sub_f32_e32 v19, v21, v5
	v_mul_f32_e32 v19, 0x3fb8aa3b, v19
	v_exp_f32_e32 v21, v19
	s_nop 0
	s_waitcnt vmcnt(50)
; #define LAS __attribute__((address_space(3)))
; DI unsigned pk2(float lo, float hi) { return cvtpk_s(lo, hi); }
; template <int SET> DI void h_prep8(const unsigned (&CR)[72], LAS unsigned char* buf, int tgp, int k2, int v64) {
;     ...
; #pragma unroll
;     for (int jp = 0; jp < 4; ++jp) {
;         float ku0[2], ku1[2];
; #pragma unroll
;         for (int jj = 0; jj < 2; ++jj) {
;             const int j = 2 * jp + jj;
;             const unsigned fw = CR[24 * SET + 8 + j], qw = CR[24 * SET + j];
;             const float f0 = __expf(bflo(fw)), f1 = __expf(bfhi(fw)), q0 = bflo(qw), q1 = bfhi(qw);
;             e20 *= f0; e21 *= f1;
;             const float e30 = __builtin_amdgcn_rcpf(e20), e31 = __builtin_amdgcn_rcpf(e21);
;             const float kk0 = 1.0f - f0, kk1 = 1.0f - f1;
;             const int t = 8 * tgp + j;
;             *(LAS unsigned*)(buf + H_QS + t * 272 + 4 * k2) = pk2(q0 * e20, q1 * e21);
;             *(LAS unsigned*)(buf + H_KS + t * 272 + 4 * k2) = pk2(kk0 * e30, kk1 * e31);
;             ku0[jj] = kk0 * e30 * elm0; ku1[jj] = kk1 * e31 * elm1;
;         }
;         kup0[jp] = pk2(ku0[0], ku0[1]); kup1[jp] = pk2(ku1[0], ku1[1]);
;     }
;     { u32x4 w; w.x = kup0[0]; w.y = kup0[1]; w.z = kup0[2]; w.w = kup0[3]; *(LAS u32x4*)(buf + H_KU + (2 * k2) * 80 + 16 * tgp) = w;
;       w.x = kup1[0]; w.y = kup1[1]; w.z = kup1[2]; w.w = kup1[3]; *(LAS u32x4*)(buf + H_KU + (2 * k2 + 1) * 80 + 16 * tgp) = w; }
;     if (tgp == 0) { *(LAS f32x2_t*)(buf + H_DEC + 8 * k2) = (f32x2_t){ebm0 * elm0, ebm1 * elm1}; *(LAS f32x2_t*)(buf + H_EBM + 8 * k2) = (f32x2_t){ebm0, ebm1}; }
	v_lshlrev_b32_e32 v19, 16, v130
	v_mul_f32_e32 v19, 0x3fb8aa3b, v19
	v_exp_f32_e32 v22, v19
	v_and_b32_e32 v19, 0xffff0000, v130
	v_mul_f32_e32 v19, 0x3fb8aa3b, v19
	v_exp_f32_e32 v23, v19
	v_lshlrev_b32_e32 v24, 16, v137
	v_and_b32_e32 v25, 0xffff0000, v137
	v_lshlrev_b32_e32 v19, 2, v6
	v_pk_mul_f32 v[20:21], v[22:23], v[20:21]
	v_mul_f32_e32 v2, 0x3fb8aa3b, v2
	v_pk_mul_f32 v[24:25], v[20:21], v[24:25]
	v_rcp_f32_e32 v26, v20
	v_cvt_pk_bf16_f32 v30, v24, v25
	v_mul_u32_u24_e32 v24, 0x880, v16
	v_add3_u32 v19, s8, v19, v24
	v_lshlrev_b32_e32 v24, 16, v132
	v_and_b32_e32 v25, 0xffff0000, v132
	v_mul_f32_e32 v24, 0x3fb8aa3b, v24
	v_mul_f32_e32 v25, 0x3fb8aa3b, v25
	v_exp_f32_e32 v24, v24
	v_exp_f32_e32 v25, v25
	v_rcp_f32_e32 v27, v21
	v_exp_f32_e32 v2, v2
	v_pk_add_f32 v[22:23], v[22:23], 1.0 op_sel_hi:[1,0] neg_lo:[1,0] neg_hi:[1,0]
	v_pk_mul_f32 v[28:29], v[24:25], v[20:21]
	v_pk_add_f32 v[24:25], v[24:25], 1.0 op_sel_hi:[1,0] neg_lo:[1,0] neg_hi:[1,0]
	v_rcp_f32_e32 v20, v28
	v_rcp_f32_e32 v21, v29
	v_pk_mul_f32 v[22:23], v[22:23], v[26:27]
	v_lshlrev_b32_e32 v26, 16, v139
	v_cvt_pk_bf16_f32 v31, v22, v23
	v_pk_mul_f32 v[20:21], v[24:25], v[20:21]
	v_and_b32_e32 v27, 0xffff0000, v139
	v_cvt_pk_bf16_f32 v24, v20, v21
	v_add_u32_e32 v34, 0x4400, v19
	v_mov_b32_e32 v25, v20
	v_mov_b32_e32 v20, v23
	v_pk_mul_f32 v[26:27], v[28:29], v[26:27]
	ds_write2_b32 v34, v31, v24 offset1:68
	v_mov_b32_e32 v24, v22
	v_pk_mul_f32 v[22:23], v[2:3], v[20:21] op_sel_hi:[0,1]
	s_nop 0
	v_lshlrev_b32_e32 v21, 16, v141
	v_cvt_pk_bf16_f32 v26, v26, v27
	v_add_u32_e32 v27, 0x2000, v19
	v_mul_f32_e32 v21, 0x3fb8aa3b, v21
	ds_write2_b32 v27, v30, v26 offset0:128 offset1:196
	v_exp_f32_e32 v26, v21
	v_and_b32_e32 v21, 0xffff0000, v141
	v_mul_f32_e32 v21, 0x3fb8aa3b, v21
	v_exp_f32_e32 v27, v21
	v_pk_mul_f32 v[24:25], v[4:5], v[24:25] op_sel_hi:[0,1]
	v_cvt_pk_bf16_f32 v20, v24, v25
	v_cvt_pk_bf16_f32 v24, v22, v23
	v_lshlrev_b32_e32 v22, 16, v136
	v_and_b32_e32 v23, 0xffff0000, v136
	v_pk_mul_f32 v[28:29], v[26:27], v[28:29]
	s_nop 0
	v_lshlrev_b32_e32 v25, 16, v158
	v_pk_mul_f32 v[22:23], v[28:29], v[22:23]
	v_mul_f32_e32 v25, 0x3fb8aa3b, v25
	v_cvt_pk_bf16_f32 v21, v22, v23
	v_pk_add_f32 v[22:23], v[26:27], 1.0 op_sel_hi:[1,0] neg_lo:[1,0] neg_hi:[1,0]
	v_exp_f32_e32 v26, v25
	v_and_b32_e32 v25, 0xffff0000, v158
	v_mul_f32_e32 v25, 0x3fb8aa3b, v25
	v_exp_f32_e32 v27, v25
	v_rcp_f32_e32 v30, v28
	v_rcp_f32_e32 v31, v29
	v_add_u32_e32 v35, 0x2400, v19
	v_pk_mul_f32 v[28:29], v[26:27], v[28:29]
	v_pk_add_f32 v[26:27], v[26:27], 1.0 op_sel_hi:[1,0] neg_lo:[1,0] neg_hi:[1,0]
	v_rcp_f32_e32 v32, v28
	v_rcp_f32_e32 v33, v29
	v_pk_mul_f32 v[22:23], v[22:23], v[30:31]
	v_lshlrev_b32_e32 v30, 16, v152
	v_and_b32_e32 v31, 0xffff0000, v152
	v_pk_mul_f32 v[30:31], v[28:29], v[30:31]
	v_pk_mul_f32 v[26:27], v[26:27], v[32:33]
	v_cvt_pk_bf16_f32 v30, v30, v31
	v_cvt_pk_bf16_f32 v25, v22, v23
	ds_write2_b32 v35, v21, v30 offset0:8 offset1:76
	v_cvt_pk_bf16_f32 v21, v26, v27
	ds_write2_b32 v34, v25, v21 offset0:136 offset1:204
	v_lshlrev_b32_e32 v25, 16, v156
	v_mov_b32_e32 v31, v26
	v_mov_b32_e32 v26, v23
	v_mul_f32_e32 v25, 0x3fb8aa3b, v25
	v_mov_b32_e32 v30, v22
	v_pk_mul_f32 v[22:23], v[2:3], v[26:27] op_sel_hi:[0,1]
	v_exp_f32_e32 v26, v25
	v_and_b32_e32 v25, 0xffff0000, v156
	v_mul_f32_e32 v25, 0x3fb8aa3b, v25
	v_exp_f32_e32 v27, v25
	v_cvt_pk_bf16_f32 v25, v22, v23
	v_lshlrev_b32_e32 v22, 16, v161
	v_and_b32_e32 v23, 0xffff0000, v161
	v_pk_mul_f32 v[28:29], v[26:27], v[28:29]
	v_pk_mul_f32 v[30:31], v[4:5], v[30:31] op_sel_hi:[0,1]
	v_pk_mul_f32 v[22:23], v[28:29], v[22:23]
	v_cvt_pk_bf16_f32 v21, v30, v31
	v_cvt_pk_bf16_f32 v34, v22, v23
	v_pk_add_f32 v[22:23], v[26:27], 1.0 op_sel_hi:[1,0] neg_lo:[1,0] neg_hi:[1,0]
	v_lshlrev_b32_e32 v26, 16, v168
	v_and_b32_e32 v27, 0xffff0000, v168
	v_mul_f32_e32 v26, 0x3fb8aa3b, v26
	v_mul_f32_e32 v27, 0x3fb8aa3b, v27
	v_exp_f32_e32 v26, v26
	v_exp_f32_e32 v27, v27
	v_rcp_f32_e32 v30, v28
	v_rcp_f32_e32 v31, v29
	v_add_u32_e32 v70, 0x4800, v19
	v_pk_mul_f32 v[28:29], v[26:27], v[28:29]
	v_pk_add_f32 v[26:27], v[26:27], 1.0 op_sel_hi:[1,0] neg_lo:[1,0] neg_hi:[1,0]
	v_rcp_f32_e32 v32, v28
	v_rcp_f32_e32 v33, v29
	v_pk_mul_f32 v[22:23], v[22:23], v[30:31]
	v_lshlrev_b32_e32 v30, 16, v163
	v_and_b32_e32 v31, 0xffff0000, v163
	v_pk_mul_f32 v[30:31], v[28:29], v[30:31]
	v_pk_mul_f32 v[26:27], v[26:27], v[32:33]
	v_cvt_pk_bf16_f32 v30, v30, v31
	v_cvt_pk_bf16_f32 v68, v22, v23
	ds_write2_b32 v35, v34, v30 offset0:144 offset1:212
	v_cvt_pk_bf16_f32 v30, v26, v27
	ds_write2_b32 v70, v68, v30 offset0:16 offset1:84
	v_mov_b32_e32 v30, v22
	v_mov_b32_e32 v31, v26
	v_mov_b32_e32 v26, v23
	s_nop 0
	v_lshlrev_b32_e32 v23, 16, v173
	v_pk_mul_f32 v[30:31], v[4:5], v[30:31] op_sel_hi:[0,1]
	v_mul_f32_e32 v23, 0x3fb8aa3b, v23
	v_cvt_pk_bf16_f32 v22, v30, v31
	v_exp_f32_e32 v30, v23
	v_and_b32_e32 v23, 0xffff0000, v173
	v_mul_f32_e32 v23, 0x3fb8aa3b, v23
	v_exp_f32_e32 v31, v23
	v_pk_mul_f32 v[26:27], v[2:3], v[26:27] op_sel_hi:[0,1]
	v_cvt_pk_bf16_f32 v26, v26, v27
	s_nop 0
	v_lshlrev_b32_e32 v32, 16, v179
	v_and_b32_e32 v33, 0xffff0000, v179
	v_pk_mul_f32 v[28:29], v[30:31], v[28:29]
	v_lshlrev_b32_e32 v27, 16, v176
	v_pk_mul_f32 v[32:33], v[28:29], v[32:33]
	v_mul_f32_e32 v27, 0x3fb8aa3b, v27
	v_cvt_pk_bf16_f32 v23, v32, v33
	v_exp_f32_e32 v32, v27
	v_and_b32_e32 v27, 0xffff0000, v176
	v_mul_f32_e32 v27, 0x3fb8aa3b, v27
	v_exp_f32_e32 v33, v27
	v_rcp_f32_e32 v34, v28
	v_rcp_f32_e32 v35, v29
	v_pk_add_f32 v[30:31], v[30:31], 1.0 op_sel_hi:[1,0] neg_lo:[1,0] neg_hi:[1,0]
	v_pk_mul_f32 v[28:29], v[32:33], v[28:29]
	v_add_u32_e32 v19, 0x2800, v19
	v_pk_mul_f32 v[30:31], v[30:31], v[34:35]
	s_nop 0
	v_lshlrev_b32_e32 v34, 16, v183
	v_and_b32_e32 v35, 0xffff0000, v183
	v_rcp_f32_e32 v68, v28
	v_rcp_f32_e32 v69, v29
	v_pk_mul_f32 v[28:29], v[28:29], v[34:35]
	v_cvt_pk_bf16_f32 v27, v30, v31
	v_cvt_pk_bf16_f32 v28, v28, v29
	ds_write2_b32 v19, v23, v28 offset0:24 offset1:92
	v_pk_add_f32 v[28:29], v[32:33], 1.0 op_sel_hi:[1,0] neg_lo:[1,0] neg_hi:[1,0]
	v_mov_b32_e32 v32, v30
	v_pk_mul_f32 v[28:29], v[28:29], v[68:69]
	s_nop 0
	v_cvt_pk_bf16_f32 v19, v28, v29
	v_mov_b32_e32 v33, v28
	v_mov_b32_e32 v28, v31
	v_pk_mul_f32 v[28:29], v[2:3], v[28:29] op_sel_hi:[0,1]
	ds_write2_b32 v70, v27, v19 offset0:152 offset1:220
	v_pk_mul_f32 v[32:33], v[4:5], v[32:33] op_sel_hi:[0,1]
	v_cvt_pk_bf16_f32 v27, v28, v29
	v_mul_u32_u24_e32 v28, 0xa0, v6
	v_lshlrev_b32_e32 v19, 4, v16
	v_cvt_pk_bf16_f32 v23, v32, v33
	v_add3_u32 v28, s8, v28, v19
	ds_write_b128 v28, v[20:23] offset:26112
	ds_write_b128 v28, v[24:27] offset:26192
	s_and_saveexec_b64 s[6:7], s[4:5]
	s_cbranch_execz .LBB0_419
	v_mul_f32_e32 v18, 0x3fb8aa3b, v18
	v_mul_f32_e32 v5, 0x3fb8aa3b, v5
	v_exp_f32_e32 v20, v18
	v_exp_f32_e32 v21, v5
	v_mov_b32_e32 v5, v2
	v_pk_mul_f32 v[4:5], v[20:21], v[4:5]
	ds_write2st64_b64 v17, v[4:5], v[20:21] offset0:81 offset1:86
; #define LAS __attribute__((address_space(3)))
; template <int SET> DI void h_totals8(const unsigned (&CR)[72], LAS unsigned char* buf, int tgp, int k2) {
;     float lo = 0.f, hi = 0.f;
; #pragma unroll
;     for (int j = 0; j < 8; ++j) { lo += bflo(CR[24 * SET + 8 + j]); hi += bfhi(CR[24 * SET + 8 + j]); }
;     *(LAS f32x2_t*)(buf + H_TOT + (tgp * 128 + 2 * k2) * 4) = (f32x2_t){lo, hi};
; }
; template <int SET> DI void h_prep8(const unsigned (&CR)[72], LAS unsigned char* buf, int tgp, int k2, int v64) {
;     ...
;     { u32x4 w; w.x = (CR[24 * SET + 16] & 0xffffu) | (CR[24 * SET + 17] << 16); w.y = (CR[24 * SET + 18] & 0xffffu) | (CR[24 * SET + 19] << 16);
;       w.z = (CR[24 * SET + 20] & 0xffffu) | (CR[24 * SET + 21] << 16); w.w = (CR[24 * SET + 22] & 0xffffu) | (CR[24 * SET + 23] << 16);
;       *(LAS u32x4*)(buf + H_VT + v64 * 80 + 16 * tgp) = w; }
.LBB0_419:
	s_or_b64 exec, exec, s[6:7]
	v_mul_u32_u24_e32 v2, 0x50, v6
	s_nop 0
	s_waitcnt vmcnt(26)
	v_lshlrev_b32_e32 v4, 16, v129
	v_and_b32_e32 v5, 0xffff0000, v129
	s_nop 0
	s_nop 0
	s_nop 0
	s_nop 0
	s_nop 0
	s_nop 0
	s_nop 0
	s_nop 0
	s_nop 0
	s_nop 0
	v_lshl_add_u32 v8, v128, 16, v126
	v_lshl_add_u32 v9, v149, 16, v147
	v_lshl_add_u32 v10, v166, 16, v154
	v_lshl_add_u32 v11, v181, 16, v170
	v_add3_u32 v2, s8, v2, v19
	v_lshlrev_b32_e32 v6, 16, v131
	v_and_b32_e32 v7, 0xffff0000, v131
	v_pk_add_f32 v[4:5], v[4:5], 0 op_sel_hi:[1,0]
	ds_write_b128 v2, v[8:11] offset:36352
	v_lshlrev_b32_e32 v8, 16, v140
	v_and_b32_e32 v9, 0xffff0000, v140
	v_pk_add_f32 v[4:5], v[4:5], v[6:7]
	v_lshlrev_b32_e32 v10, 16, v157
	v_and_b32_e32 v11, 0xffff0000, v157
	v_pk_add_f32 v[4:5], v[4:5], v[8:9]
	s_nop 0
	s_nop 0
	s_nop 0
	s_nop 0
	v_lshlrev_b32_e32 v12, 16, v155
	v_and_b32_e32 v13, 0xffff0000, v155
	v_pk_add_f32 v[4:5], v[4:5], v[10:11]
	s_bitcmp1_b32 s39, 0
	v_lshlrev_b32_e32 v18, 16, v167
	v_and_b32_e32 v19, 0xffff0000, v167
	v_pk_add_f32 v[4:5], v[4:5], v[12:13]
	s_cselect_b32 s4, 0xb400, 0
	v_lshlrev_b32_e32 v20, 16, v172
	v_and_b32_e32 v21, 0xffff0000, v172
	v_pk_add_f32 v[4:5], v[4:5], v[18:19]
	s_add_i32 s4, s4, 0
	v_lshlrev_b32_e32 v22, 16, v175
	v_and_b32_e32 v23, 0xffff0000, v175
	v_pk_add_f32 v[4:5], v[4:5], v[20:21]
	v_lshlrev_b32_e32 v2, 9, v16
	v_pk_add_f32 v[4:5], v[4:5], v[22:23]
	v_add3_u32 v2, s4, v2, v15
	s_nop 0
	s_nop 0
	ds_write_b64 v2, v[4:5] offset:41984
	v_mov_b64_e32 v[4:5], v[36:37]
	v_mov_b64_e32 v[20:21], v[52:53]
	v_mov_b64_e32 v[6:7], v[38:39]
	v_mov_b64_e32 v[8:9], v[40:41]
	v_mov_b64_e32 v[10:11], v[42:43]
	v_mov_b64_e32 v[12:13], v[44:45]
	v_mov_b64_e32 v[14:15], v[46:47]
	v_mov_b64_e32 v[16:17], v[48:49]
	v_mov_b64_e32 v[18:19], v[50:51]
	v_mov_b64_e32 v[22:23], v[54:55]
	v_mov_b64_e32 v[24:25], v[56:57]
	v_mov_b64_e32 v[26:27], v[58:59]
	v_mov_b64_e32 v[28:29], v[60:61]
	v_mov_b64_e32 v[30:31], v[62:63]
	v_mov_b64_e32 v[32:33], v[64:65]
	v_mov_b64_e32 v[34:35], v[66:67]

; #define LAS __attribute__((address_space(3)))
; DI unsigned pk2(float lo, float hi) { return cvtpk_s(lo, hi); }
; DI int opaque_tid() { int t = threadIdx.x; asm volatile("" : "+v"(t)); return t; }
; template <int SET> DI void h_load8(unsigned (&CR)[72], const bf16_t* qp, const bf16_t* fp, const bf16_t* ip, int c) {
; #pragma unroll
;     for (int j = 0; j < 8; ++j) { const size_t ro = (size_t)(32 * c + j) * D; CR[24 * SET + j] = *(const unsigned*)(qp + ro); CR[24 * SET + 8 + j] = *(const unsigned*)(fp + ro); CR[24 * SET + 16 + j] = ip[ro]; }
; }
; DI void h_reduce_store2(LAS unsigned char* red, bf16_t* op, int c, int pt) {
; #pragma unroll
;     for (int s2 = 0; s2 < 2; ++s2) {
;         const int s = pt + 256 * s2, t = s >> 4, c4 = s & 15;
;         const f32x4 a = *(const LAS f32x4*)(red + ((0 * 32 + t) * 64 + 4 * c4) * 4), b2 = *(const LAS f32x4*)(red + ((1 * 32 + t) * 64 + 4 * c4) * 4);
;         const f32x4 sm = a + b2;
;         u32x2 w; w.x = pk2(sm[0], sm[1]); w.y = pk2(sm[2], sm[3]);
;         *(u32x2*)(op + (size_t)(32 * c + t) * D + 4 * c4) = w;
;     }
; }
; template <int RF, int RN, int RNN> DI void h_prep_step(unsigned (&CR)[72], ArgsP A, LAS unsigned char* lds, int cc, size_t rb, int h, int vhalf) {
;     const int pt = opaque_tid() & 255, k2 = pt & 63, tgp = pt >> 6, v64 = pt & 63;
;     const bf16_t* QA = (const bf16_t*)(A->ws + WS_QA); const bf16_t* LF = (const bf16_t*)(A->ws + WS_LF); const bf16_t* IA = (const bf16_t*)(A->ws + WS_IA); bf16_t* OH = (bf16_t*)(A->ws + WS_OH);
;     if (cc + 3 < 64) {
;         const bf16_t* qp = QA + rb + (size_t)(8 * tgp) * D + h * 128 + 2 * k2; const bf16_t* fp = LF + rb + (size_t)(8 * tgp) * D + h * 128 + 2 * k2;
;         const bf16_t* ip = IA + rb + (size_t)(8 * tgp) * D + h * 128 + vhalf * 64 + v64;
;         h_load8<RF>(CR, qp, fp, ip, cc + 3);
;     }
;     if (cc >= 1) h_reduce_store2(lds + H_RED2 + ((cc - 1) & 1) * 16384, OH + rb + h * 128 + vhalf * 64, cc - 1, pt);
;     if (cc + 1 < 64) h_prep8<RN>(CR, lds + ((cc + 1) & 1) * H_BUF, tgp, k2, v64);
;     if (cc + 2 < 64) h_totals8<RNN>(CR, lds + ((cc + 2) & 1) * H_BUF, tgp, k2);
; }
.LBB0_422:
	s_andn2_b64 vcc, exec, s[4:5]
	s_cbranch_vccnz .LBB0_428
	v_mov_b32_e32 v36, v0
	s_load_dwordx2 s[4:5], s[40:41], 0x98
	s_cmp_gt_u32 s39, 59
	v_and_b32_e32 v38, 63, v36
	s_cbranch_scc1 .Lp2_skip_b
	s_waitcnt lgkmcnt(0)
	s_add_u32 s98, s4, s54
	s_addc_u32 s99, s5, s55
	s_add_u32 s98, s98, s56
	s_addc_u32 s99, s99, s57
	s_add_u32 s98, s98, 0xa280000
	s_addc_u32 s99, s99, 0
	v_lshlrev_b32_e32 v2, 9, v36
	v_and_b32_e32 v37, 0x18000, v2
	v_lshl_or_b32 v2, v38, 2, v37
	v_lshl_or_b32 v2, v38, 1, v37
	global_load_dword v137, v200, s[98:99]
	global_load_dword v139, v201, s[98:99]
	global_load_dword v136, v202, s[98:99]
	global_load_dword v152, v203, s[98:99]
	global_load_dword v161, v204, s[98:99]
	global_load_dword v163, v205, s[98:99]
	global_load_dword v179, v206, s[98:99]
	global_load_dword v183, v207, s[98:99]
	s_add_u32 s98, s98, 0x4000000
	s_addc_u32 s99, s99, 0
	global_load_dword v130, v200, s[98:99]
	global_load_dword v132, v201, s[98:99]
	global_load_dword v141, v202, s[98:99]
	global_load_dword v158, v203, s[98:99]
	global_load_dword v156, v204, s[98:99]
	global_load_dword v168, v205, s[98:99]
	global_load_dword v173, v206, s[98:99]
	global_load_dword v176, v207, s[98:99]
	s_add_u32 s98, s98, 0x4000000
	s_addc_u32 s99, s99, 0
	global_load_ushort v126, v208, s[98:99]
	global_load_ushort v128, v209, s[98:99]
	global_load_ushort v147, v210, s[98:99]
	global_load_ushort v149, v211, s[98:99]
	global_load_ushort v154, v212, s[98:99]
	global_load_ushort v166, v213, s[98:99]
	global_load_ushort v170, v214, s[98:99]
	global_load_ushort v181, v215, s[98:99]
.LBB0_425:
	s_add_i32 s6, s38, 0x4000
	s_and_b32 s6, s6, 0x4000
	s_add_i32 s6, s6, 0
	s_add_i32 s8, s39, 1
	s_add_i32 s9, s6, 0x16800
	s_lshl_b64 s[6:7], s[52:53], 1
	s_waitcnt lgkmcnt(0)
	s_add_u32 s4, s4, s6
	s_addc_u32 s5, s5, s7
	s_lshl_b32 s6, s96, 1
	v_lshlrev_b32_e32 v2, 2, v36
	s_add_u32 s4, s4, s6
	v_and_b32_e32 v2, 60, v2
	v_bfe_u32 v58, v36, 4, 4
	s_addc_u32 s5, s5, 0
	s_lshl_b32 s6, s48, 1
	v_lshlrev_b32_e32 v37, 2, v2
	v_lshlrev_b32_e32 v40, 8, v58
	s_add_u32 s4, s4, s6
	v_add3_u32 v37, s9, v37, v40
	s_addc_u32 s5, s5, 0
	v_lshlrev_b32_e32 v2, 1, v2
	ds_read_b128 v[40:43], v37
	ds_read_b128 v[44:47], v37 offset:8192
	v_lshl_add_u64 v[48:49], s[4:5], 0, v[2:3]
	v_lshl_add_u64 v[56:57], v[48:49], 0, s[50:51]
	ds_read_b128 v[48:51], v37 offset:4096
	ds_read_b128 v[52:55], v37 offset:12288
	v_lshl_add_u32 v37, v58, 11, s97
	s_waitcnt lgkmcnt(2)
	v_pk_add_f32 v[42:43], v[42:43], v[46:47]
	v_pk_add_f32 v[40:41], v[40:41], v[44:45]
	v_add_u32_e32 v2, 0x10000, v37
	v_cvt_pk_bf16_f32 v40, v40, v41
	v_cvt_pk_bf16_f32 v41, v42, v43
	v_lshl_add_u64 v[42:43], v[2:3], 1, v[56:57]
	s_andn2_b32 s4, 1, s8
	global_store_dwordx2 v[42:43], v[40:41], off
	s_waitcnt lgkmcnt(0)
	v_pk_add_f32 v[40:41], v[50:51], v[54:55]
	s_mul_i32 s4, s4, 0xb400
	v_cvt_pk_bf16_f32 v47, v40, v41
	s_add_i32 s9, s4, 0
	v_lshlrev_b32_e32 v40, 3, v38
	v_pk_add_f32 v[42:43], v[48:49], v[52:53]
	v_add_u32_e32 v41, s9, v40
	v_cvt_pk_bf16_f32 v46, v42, v43
	ds_read2st64_b64 v[42:45], v41 offset0:82 offset1:83
	v_add_u32_e32 v2, 0x18000, v37
	v_lshl_add_u64 v[48:49], v[2:3], 1, v[56:57]
	global_store_dwordx2 v[48:49], v[46:47], off
	ds_read2st64_b64 v[46:49], v41 offset0:84 offset1:85
	s_waitcnt lgkmcnt(1)
	v_add_f32_e32 v2, 0, v42
	v_cmp_lt_u32_sdwa s[4:5], v36, v120 src0_sel:BYTE_0 src1_sel:DWORD
	v_add_f32_e32 v37, 0, v43
	v_cmp_gt_u32_sdwa vcc, v36, s88 src0_sel:BYTE_0 src1_sel:DWORD
	v_cndmask_b32_e64 v43, v2, 0, s[4:5]
	v_cndmask_b32_e64 v42, v37, 0, s[4:5]
	v_add_f32_e32 v50, v44, v43
	v_bfe_u32 v39, v36, 6, 2
	v_add_f32_e32 v51, v45, v42
	v_cndmask_b32_e32 v43, v43, v50, vcc
	v_cndmask_b32_e32 v36, v42, v51, vcc
	v_add_f32_e32 v42, v2, v44
	s_waitcnt lgkmcnt(0)
	v_add_f32_e32 v2, v46, v43
	v_cmp_eq_u32_e32 vcc, 3, v39
	v_add_f32_e32 v37, v37, v45
	v_add_f32_e32 v44, v47, v36
	v_cndmask_b32_e32 v43, v43, v2, vcc
	v_add_f32_e32 v2, v42, v46
	v_add_f32_e32 v2, v2, v48
	v_cndmask_b32_e32 v45, v36, v44, vcc
	v_add_f32_e32 v36, v37, v47
	v_sub_f32_e32 v2, v2, v42
	v_sub_f32_e32 v43, v43, v42
	v_add_f32_e32 v44, v36, v49
	v_mul_f32_e32 v2, 0x3fb8aa3b, v2
	v_mul_f32_e32 v43, 0x3fb8aa3b, v43
	v_exp_f32_e32 v36, v2
	v_sub_f32_e32 v2, v44, v37
	v_exp_f32_e32 v44, v43
	v_sub_f32_e32 v43, v45, v37
	v_mul_f32_e32 v43, 0x3fb8aa3b, v43
	v_exp_f32_e32 v45, v43
	s_nop 0
	s_waitcnt vmcnt(50)
; template <int SET> DI void h_prep8(const unsigned (&CR)[72], LAS unsigned char* buf, int tgp, int k2, int v64) {
;     float base0 = 0.f, base1 = 0.f, bm0 = 0.f, bm1 = 0.f, bl0 = 0.f, bl1 = 0.f;
; #pragma unroll
;     for (int g = 0; g < 4; ++g) { const f32x2_t tt = *(const LAS f32x2_t*)(buf + H_TOT + (g * 128 + 2 * k2) * 4);
;         if (g < tgp) { base0 += tt[0]; base1 += tt[1]; } if (g < 2) { bm0 += tt[0]; bm1 += tt[1]; } bl0 += tt[0]; bl1 += tt[1]; }
;     const float ebm0 = __expf(bm0), ebm1 = __expf(bm1), elm0 = __expf(bl0 - bm0), elm1 = __expf(bl1 - bm1);
;     float e20 = __expf(base0 - bm0), e21 = __expf(base1 - bm1); unsigned kup0[4], kup1[4];
; #pragma unroll
;     for (int jp = 0; jp < 4; ++jp) {
;         float ku0[2], ku1[2];
; #pragma unroll
;         for (int jj = 0; jj < 2; ++jj) {
;             const int j = 2 * jp + jj;
;             const unsigned fw = CR[24 * SET + 8 + j], qw = CR[24 * SET + j];
;             const float f0 = __expf(bflo(fw)), f1 = __expf(bfhi(fw)), q0 = bflo(qw), q1 = bfhi(qw);
;             e20 *= f0; e21 *= f1;
;             const float e30 = __builtin_amdgcn_rcpf(e20), e31 = __builtin_amdgcn_rcpf(e21);
;             const float kk0 = 1.0f - f0, kk1 = 1.0f - f1;
;             const int t = 8 * tgp + j;
;             *(LAS unsigned*)(buf + H_QS + t * 272 + 4 * k2) = pk2(q0 * e20, q1 * e21);
;             *(LAS unsigned*)(buf + H_KS + t * 272 + 4 * k2) = pk2(kk0 * e30, kk1 * e31);
;             ku0[jj] = kk0 * e30 * elm0; ku1[jj] = kk1 * e31 * elm1;
;         }
;         kup0[jp] = pk2(ku0[0], ku0[1]); kup1[jp] = pk2(ku1[0], ku1[1]);
;     }
;     { u32x4 w; w.x = kup0[0]; w.y = kup0[1]; w.z = kup0[2]; w.w = kup0[3]; *(LAS u32x4*)(buf + H_KU + (2 * k2) * 80 + 16 * tgp) = w;
;       w.x = kup1[0]; w.y = kup1[1]; w.z = kup1[2]; w.w = kup1[3]; *(LAS u32x4*)(buf + H_KU + (2 * k2 + 1) * 80 + 16 * tgp) = w; }
;     if (tgp == 0) { *(LAS f32x2_t*)(buf + H_DEC + 8 * k2) = (f32x2_t){ebm0 * elm0, ebm1 * elm1}; *(LAS f32x2_t*)(buf + H_EBM + 8 * k2) = (f32x2_t){ebm0, ebm1}; }
;     { u32x4 w; w.x = (CR[24 * SET + 16] & 0xffffu) | (CR[24 * SET + 17] << 16); w.y = (CR[24 * SET + 18] & 0xffffu) | (CR[24 * SET + 19] << 16);
;       w.z = (CR[24 * SET + 20] & 0xffffu) | (CR[24 * SET + 21] << 16); w.w = (CR[24 * SET + 22] & 0xffffu) | (CR[24 * SET + 23] << 16);
;       *(LAS u32x4*)(buf + H_VT + v64 * 80 + 16 * tgp) = w; }
; }
	v_lshlrev_b32_e32 v43, 16, v129
	v_mul_f32_e32 v43, 0x3fb8aa3b, v43
	v_exp_f32_e32 v46, v43
	v_and_b32_e32 v43, 0xffff0000, v129
	v_mul_f32_e32 v43, 0x3fb8aa3b, v43
	v_exp_f32_e32 v47, v43
	s_nop 0
	v_lshlrev_b32_e32 v48, 16, v135
	v_and_b32_e32 v49, 0xffff0000, v135
	v_lshlrev_b32_e32 v43, 2, v38
	v_pk_mul_f32 v[44:45], v[46:47], v[44:45]
	v_mul_f32_e32 v2, 0x3fb8aa3b, v2
	v_pk_mul_f32 v[48:49], v[44:45], v[48:49]
	v_rcp_f32_e32 v50, v44
	v_cvt_pk_bf16_f32 v54, v48, v49
	v_mul_u32_u24_e32 v48, 0x880, v39
	v_add3_u32 v43, s9, v43, v48
	v_lshlrev_b32_e32 v48, 16, v131
	v_and_b32_e32 v49, 0xffff0000, v131
	v_mul_f32_e32 v48, 0x3fb8aa3b, v48
	v_mul_f32_e32 v49, 0x3fb8aa3b, v49
	v_exp_f32_e32 v48, v48
	v_exp_f32_e32 v49, v49
	v_rcp_f32_e32 v51, v45
	v_exp_f32_e32 v2, v2
	v_pk_add_f32 v[46:47], v[46:47], 1.0 op_sel_hi:[1,0] neg_lo:[1,0] neg_hi:[1,0]
	v_pk_mul_f32 v[52:53], v[48:49], v[44:45]
	v_pk_add_f32 v[48:49], v[48:49], 1.0 op_sel_hi:[1,0] neg_lo:[1,0] neg_hi:[1,0]
	v_rcp_f32_e32 v44, v52
	v_rcp_f32_e32 v45, v53
	v_pk_mul_f32 v[46:47], v[46:47], v[50:51]
	s_nop 0
	v_lshlrev_b32_e32 v50, 16, v138
	v_cvt_pk_bf16_f32 v55, v46, v47
	v_pk_mul_f32 v[44:45], v[48:49], v[44:45]
	v_and_b32_e32 v51, 0xffff0000, v138
	v_cvt_pk_bf16_f32 v48, v44, v45
	v_add_u32_e32 v58, 0x4400, v43
	v_mov_b32_e32 v49, v44
	v_mov_b32_e32 v44, v47
	v_pk_mul_f32 v[50:51], v[52:53], v[50:51]
	ds_write2_b32 v58, v55, v48 offset1:68
	v_mov_b32_e32 v48, v46
	v_pk_mul_f32 v[46:47], v[2:3], v[44:45] op_sel_hi:[0,1]
	s_nop 0
	v_lshlrev_b32_e32 v45, 16, v140
	v_cvt_pk_bf16_f32 v50, v50, v51
	v_add_u32_e32 v51, 0x2000, v43
	v_mul_f32_e32 v45, 0x3fb8aa3b, v45
	ds_write2_b32 v51, v54, v50 offset0:128 offset1:196
	v_exp_f32_e32 v50, v45
	v_and_b32_e32 v45, 0xffff0000, v140
	v_mul_f32_e32 v45, 0x3fb8aa3b, v45
	v_exp_f32_e32 v51, v45
	v_pk_mul_f32 v[48:49], v[36:37], v[48:49] op_sel_hi:[0,1]
	v_cvt_pk_bf16_f32 v44, v48, v49
	v_cvt_pk_bf16_f32 v48, v46, v47
	v_lshlrev_b32_e32 v46, 16, v134
	v_and_b32_e32 v47, 0xffff0000, v134
	v_pk_mul_f32 v[52:53], v[50:51], v[52:53]
	s_nop 0
	v_lshlrev_b32_e32 v49, 16, v157
	v_pk_mul_f32 v[46:47], v[52:53], v[46:47]
	v_mul_f32_e32 v49, 0x3fb8aa3b, v49
	v_cvt_pk_bf16_f32 v45, v46, v47
	v_pk_add_f32 v[46:47], v[50:51], 1.0 op_sel_hi:[1,0] neg_lo:[1,0] neg_hi:[1,0]
	v_exp_f32_e32 v50, v49
	v_and_b32_e32 v49, 0xffff0000, v157
	v_mul_f32_e32 v49, 0x3fb8aa3b, v49
	v_exp_f32_e32 v51, v49
	v_rcp_f32_e32 v54, v52
	v_rcp_f32_e32 v55, v53
	v_add_u32_e32 v59, 0x2400, v43
	v_pk_mul_f32 v[52:53], v[50:51], v[52:53]
	v_pk_add_f32 v[50:51], v[50:51], 1.0 op_sel_hi:[1,0] neg_lo:[1,0] neg_hi:[1,0]
	v_rcp_f32_e32 v56, v52
	v_rcp_f32_e32 v57, v53
	v_pk_mul_f32 v[46:47], v[46:47], v[54:55]
	v_lshlrev_b32_e32 v54, 16, v151
	v_and_b32_e32 v55, 0xffff0000, v151
	v_pk_mul_f32 v[54:55], v[52:53], v[54:55]
	v_pk_mul_f32 v[50:51], v[50:51], v[56:57]
	v_cvt_pk_bf16_f32 v54, v54, v55
	v_cvt_pk_bf16_f32 v49, v46, v47
	ds_write2_b32 v59, v45, v54 offset0:8 offset1:76
	v_cvt_pk_bf16_f32 v45, v50, v51
	ds_write2_b32 v58, v49, v45 offset0:136 offset1:204
	v_lshlrev_b32_e32 v49, 16, v155
	v_mov_b32_e32 v55, v50
	v_mov_b32_e32 v50, v47
	v_mul_f32_e32 v49, 0x3fb8aa3b, v49
	v_mov_b32_e32 v54, v46
	v_pk_mul_f32 v[46:47], v[2:3], v[50:51] op_sel_hi:[0,1]
	v_exp_f32_e32 v50, v49
	v_and_b32_e32 v49, 0xffff0000, v155
	v_mul_f32_e32 v49, 0x3fb8aa3b, v49
	v_exp_f32_e32 v51, v49
	v_cvt_pk_bf16_f32 v49, v46, v47
	v_lshlrev_b32_e32 v46, 16, v160
	v_and_b32_e32 v47, 0xffff0000, v160
	v_pk_mul_f32 v[52:53], v[50:51], v[52:53]
	v_pk_mul_f32 v[54:55], v[36:37], v[54:55] op_sel_hi:[0,1]
	v_pk_mul_f32 v[46:47], v[52:53], v[46:47]
	v_cvt_pk_bf16_f32 v45, v54, v55
	v_cvt_pk_bf16_f32 v58, v46, v47
	v_pk_add_f32 v[46:47], v[50:51], 1.0 op_sel_hi:[1,0] neg_lo:[1,0] neg_hi:[1,0]
	v_lshlrev_b32_e32 v50, 16, v167
	v_and_b32_e32 v51, 0xffff0000, v167
	v_mul_f32_e32 v50, 0x3fb8aa3b, v50
	v_mul_f32_e32 v51, 0x3fb8aa3b, v51
	v_exp_f32_e32 v50, v50
	v_exp_f32_e32 v51, v51
	v_rcp_f32_e32 v54, v52
	v_rcp_f32_e32 v55, v53
	v_add_u32_e32 v62, 0x4800, v43
	v_pk_mul_f32 v[52:53], v[50:51], v[52:53]
	v_pk_add_f32 v[50:51], v[50:51], 1.0 op_sel_hi:[1,0] neg_lo:[1,0] neg_hi:[1,0]
	v_rcp_f32_e32 v56, v52
	v_rcp_f32_e32 v57, v53
	v_pk_mul_f32 v[46:47], v[46:47], v[54:55]
	v_lshlrev_b32_e32 v54, 16, v162
	v_and_b32_e32 v55, 0xffff0000, v162
	v_pk_mul_f32 v[54:55], v[52:53], v[54:55]
	v_pk_mul_f32 v[50:51], v[50:51], v[56:57]
	v_cvt_pk_bf16_f32 v54, v54, v55
	v_cvt_pk_bf16_f32 v60, v46, v47
	ds_write2_b32 v59, v58, v54 offset0:144 offset1:212
	v_cvt_pk_bf16_f32 v54, v50, v51
	ds_write2_b32 v62, v60, v54 offset0:16 offset1:84
	v_mov_b32_e32 v54, v46
	v_mov_b32_e32 v55, v50
	v_mov_b32_e32 v50, v47
	s_nop 0
	v_lshlrev_b32_e32 v47, 16, v172
	v_pk_mul_f32 v[54:55], v[36:37], v[54:55] op_sel_hi:[0,1]
	v_mul_f32_e32 v47, 0x3fb8aa3b, v47
	v_cvt_pk_bf16_f32 v46, v54, v55
	v_exp_f32_e32 v54, v47
	v_and_b32_e32 v47, 0xffff0000, v172
	v_mul_f32_e32 v47, 0x3fb8aa3b, v47
	v_exp_f32_e32 v55, v47
	v_pk_mul_f32 v[50:51], v[2:3], v[50:51] op_sel_hi:[0,1]
	v_cvt_pk_bf16_f32 v50, v50, v51
	s_nop 0
	v_lshlrev_b32_e32 v56, 16, v178
	v_and_b32_e32 v57, 0xffff0000, v178
	v_pk_mul_f32 v[52:53], v[54:55], v[52:53]
	v_lshlrev_b32_e32 v51, 16, v175
	v_pk_mul_f32 v[56:57], v[52:53], v[56:57]
	v_mul_f32_e32 v51, 0x3fb8aa3b, v51
	v_cvt_pk_bf16_f32 v47, v56, v57
	v_exp_f32_e32 v56, v51
	v_and_b32_e32 v51, 0xffff0000, v175
	v_mul_f32_e32 v51, 0x3fb8aa3b, v51
	v_exp_f32_e32 v57, v51
	v_rcp_f32_e32 v58, v52
	v_rcp_f32_e32 v59, v53
	v_pk_add_f32 v[54:55], v[54:55], 1.0 op_sel_hi:[1,0] neg_lo:[1,0] neg_hi:[1,0]
	v_pk_mul_f32 v[52:53], v[56:57], v[52:53]
	v_add_u32_e32 v43, 0x2800, v43
	v_pk_mul_f32 v[54:55], v[54:55], v[58:59]
	s_nop 0
	v_lshlrev_b32_e32 v58, 16, v182
	v_and_b32_e32 v59, 0xffff0000, v182
	v_rcp_f32_e32 v60, v52
	v_rcp_f32_e32 v61, v53
	v_pk_mul_f32 v[52:53], v[52:53], v[58:59]
	v_cvt_pk_bf16_f32 v51, v54, v55
	v_cvt_pk_bf16_f32 v52, v52, v53
	ds_write2_b32 v43, v47, v52 offset0:24 offset1:92
	v_pk_add_f32 v[52:53], v[56:57], 1.0 op_sel_hi:[1,0] neg_lo:[1,0] neg_hi:[1,0]
	v_mov_b32_e32 v56, v54
	v_pk_mul_f32 v[52:53], v[52:53], v[60:61]
	s_nop 0
	v_cvt_pk_bf16_f32 v43, v52, v53
	v_mov_b32_e32 v57, v52
	v_mov_b32_e32 v52, v55
	v_pk_mul_f32 v[52:53], v[2:3], v[52:53] op_sel_hi:[0,1]
	ds_write2_b32 v62, v51, v43 offset0:152 offset1:220
	v_pk_mul_f32 v[56:57], v[36:37], v[56:57] op_sel_hi:[0,1]
	v_cvt_pk_bf16_f32 v51, v52, v53
	v_mul_u32_u24_e32 v52, 0xa0, v38
	v_lshlrev_b32_e32 v43, 4, v39
	v_cvt_pk_bf16_f32 v47, v56, v57
	v_add3_u32 v52, s9, v52, v43
	ds_write_b128 v52, v[44:47] offset:26112
	ds_write_b128 v52, v[48:51] offset:26192
	s_and_saveexec_b64 s[6:7], s[4:5]
	s_cbranch_execz .LBB0_427
	v_mul_f32_e32 v42, 0x3fb8aa3b, v42
	v_mul_f32_e32 v37, 0x3fb8aa3b, v37
	v_exp_f32_e32 v44, v42
	v_exp_f32_e32 v45, v37
	v_mov_b32_e32 v37, v2
	v_pk_mul_f32 v[36:37], v[44:45], v[36:37]
	ds_write2st64_b64 v41, v[36:37], v[44:45] offset0:81 offset1:86
; #define LAS __attribute__((address_space(3)))
; template <int SET> DI void h_totals8(const unsigned (&CR)[72], LAS unsigned char* buf, int tgp, int k2) {
;     float lo = 0.f, hi = 0.f;
; #pragma unroll
;     for (int j = 0; j < 8; ++j) { lo += bflo(CR[24 * SET + 8 + j]); hi += bfhi(CR[24 * SET + 8 + j]); }
;     *(LAS f32x2_t*)(buf + H_TOT + (tgp * 128 + 2 * k2) * 4) = (f32x2_t){lo, hi};
; }
; template <int SET> DI void h_prep8(const unsigned (&CR)[72], LAS unsigned char* buf, int tgp, int k2, int v64) {
;     ...
;     { u32x4 w; w.x = (CR[24 * SET + 16] & 0xffffu) | (CR[24 * SET + 17] << 16); w.y = (CR[24 * SET + 18] & 0xffffu) | (CR[24 * SET + 19] << 16);
;       w.z = (CR[24 * SET + 20] & 0xffffu) | (CR[24 * SET + 21] << 16); w.w = (CR[24 * SET + 22] & 0xffffu) | (CR[24 * SET + 23] << 16);
;       *(LAS u32x4*)(buf + H_VT + v64 * 80 + 16 * tgp) = w; }
.LBB0_427:
	s_or_b64 exec, exec, s[6:7]
	v_mul_u32_u24_e32 v2, 0x50, v38
	s_waitcnt vmcnt(26)
	v_lshlrev_b32_e32 v36, 16, v121
	v_and_b32_e32 v37, 0xffff0000, v121
	v_lshl_add_u32 v44, v127, 16, v125
	v_lshl_add_u32 v45, v148, 16, v146
	v_lshl_add_u32 v46, v165, 16, v153
	v_lshl_add_u32 v47, v180, 16, v169
	v_add3_u32 v2, s9, v2, v43
	v_lshlrev_b32_e32 v42, 16, v122
	v_and_b32_e32 v43, 0xffff0000, v122
	v_pk_add_f32 v[36:37], v[36:37], 0 op_sel_hi:[1,0]
	ds_write_b128 v2, v[44:47] offset:36352
	v_lshlrev_b32_e32 v44, 16, v133
	v_and_b32_e32 v45, 0xffff0000, v133
	v_pk_add_f32 v[36:37], v[36:37], v[42:43]
	v_lshlrev_b32_e32 v46, 16, v144
	v_and_b32_e32 v47, 0xffff0000, v144
	v_pk_add_f32 v[36:37], v[36:37], v[44:45]
	v_lshlrev_b32_e32 v48, 16, v150
	v_and_b32_e32 v49, 0xffff0000, v150
	v_pk_add_f32 v[36:37], v[36:37], v[46:47]
	s_bitcmp1_b32 s8, 0
	v_lshlrev_b32_e32 v50, 16, v164
	v_and_b32_e32 v51, 0xffff0000, v164
	v_pk_add_f32 v[36:37], v[36:37], v[48:49]
	s_cselect_b32 s4, 0xb400, 0
	v_lshlrev_b32_e32 v52, 16, v171
	v_and_b32_e32 v53, 0xffff0000, v171
	v_pk_add_f32 v[36:37], v[36:37], v[50:51]
	s_add_i32 s4, s4, 0
	v_lshlrev_b32_e32 v54, 16, v174
	v_and_b32_e32 v55, 0xffff0000, v174
	v_pk_add_f32 v[36:37], v[36:37], v[52:53]
	v_lshlrev_b32_e32 v2, 9, v39
	v_pk_add_f32 v[36:37], v[36:37], v[54:55]
	v_add3_u32 v2, s4, v2, v40
	ds_write_b64 v2, v[36:37] offset:41984
	s_branch .LBB0_429
.Lp2_skip_b:
	s_waitcnt vmcnt(0)
	s_branch .LBB0_425

; #define LAS __attribute__((address_space(3)))
; DI unsigned pk2(float lo, float hi) { return cvtpk_s(lo, hi); }
; template <int SET> DI void h_load8(unsigned (&CR)[72], const bf16_t* qp, const bf16_t* fp, const bf16_t* ip, int c) {
; #pragma unroll
;     for (int j = 0; j < 8; ++j) { const size_t ro = (size_t)(32 * c + j) * D; CR[24 * SET + j] = *(const unsigned*)(qp + ro); CR[24 * SET + 8 + j] = *(const unsigned*)(fp + ro); CR[24 * SET + 16 + j] = ip[ro]; }
; }
; template <int SET> DI void h_prep8(const unsigned (&CR)[72], LAS unsigned char* buf, int tgp, int k2, int v64) {
;     float base0 = 0.f, base1 = 0.f, bm0 = 0.f, bm1 = 0.f, bl0 = 0.f, bl1 = 0.f;
; #pragma unroll
;     for (int g = 0; g < 4; ++g) { const f32x2_t tt = *(const LAS f32x2_t*)(buf + H_TOT + (g * 128 + 2 * k2) * 4);
;         if (g < tgp) { base0 += tt[0]; base1 += tt[1]; } if (g < 2) { bm0 += tt[0]; bm1 += tt[1]; } bl0 += tt[0]; bl1 += tt[1]; }
;     const float ebm0 = __expf(bm0), ebm1 = __expf(bm1), elm0 = __expf(bl0 - bm0), elm1 = __expf(bl1 - bm1);
; DI void h_reduce_store2(LAS unsigned char* red, bf16_t* op, int c, int pt) {
; #pragma unroll
;     for (int s2 = 0; s2 < 2; ++s2) {
;         const int s = pt + 256 * s2, t = s >> 4, c4 = s & 15;
;         const f32x4 a = *(const LAS f32x4*)(red + ((0 * 32 + t) * 64 + 4 * c4) * 4), b2 = *(const LAS f32x4*)(red + ((1 * 32 + t) * 64 + 4 * c4) * 4);
;         const f32x4 sm = a + b2;
;         u32x2 w; w.x = pk2(sm[0], sm[1]); w.y = pk2(sm[2], sm[3]);
;         *(u32x2*)(op + (size_t)(32 * c + t) * D + 4 * c4) = w;
;     }
; }
.LBB0_431:
	s_andn2_b64 vcc, exec, s[4:5]
	s_cbranch_vccnz .LBB0_438
	v_mov_b32_e32 v36, v0
	s_load_dwordx2 s[4:5], s[40:41], 0x98
	s_cmp_gt_u32 s39, 58
	v_and_b32_e32 v38, 63, v36
	s_cbranch_scc1 .Lp2_skip_c
	s_waitcnt lgkmcnt(0)
	s_add_u32 s98, s4, s54
	s_addc_u32 s99, s5, s55
	s_add_u32 s98, s98, s56
	s_addc_u32 s99, s99, s57
	s_add_u32 s98, s98, 0xa2a0000
	s_addc_u32 s99, s99, 0
	v_lshlrev_b32_e32 v2, 9, v36
	v_and_b32_e32 v37, 0x18000, v2
	v_lshl_or_b32 v2, v38, 2, v37
	v_lshl_or_b32 v2, v38, 1, v37
	global_load_dword v135, v200, s[98:99]
	global_load_dword v138, v201, s[98:99]
	global_load_dword v134, v202, s[98:99]
	global_load_dword v151, v203, s[98:99]
	global_load_dword v160, v204, s[98:99]
	global_load_dword v162, v205, s[98:99]
	global_load_dword v178, v206, s[98:99]
	global_load_dword v182, v207, s[98:99]
	s_add_u32 s98, s98, 0x4000000
	s_addc_u32 s99, s99, 0
	global_load_dword v129, v200, s[98:99]
	global_load_dword v131, v201, s[98:99]
	global_load_dword v140, v202, s[98:99]
	global_load_dword v157, v203, s[98:99]
	global_load_dword v155, v204, s[98:99]
	global_load_dword v167, v205, s[98:99]
	global_load_dword v172, v206, s[98:99]
	global_load_dword v175, v207, s[98:99]
	s_add_u32 s98, s98, 0x4000000
	s_addc_u32 s99, s99, 0
	global_load_ushort v125, v208, s[98:99]
	global_load_ushort v127, v209, s[98:99]
	global_load_ushort v146, v210, s[98:99]
	global_load_ushort v148, v211, s[98:99]
	global_load_ushort v153, v212, s[98:99]
	global_load_ushort v165, v213, s[98:99]
	global_load_ushort v169, v214, s[98:99]
	global_load_ushort v180, v215, s[98:99]
.LBB0_434:
	s_add_i32 s6, s38, 0x8000
	s_and_b32 s6, s6, 0x4000
	s_add_i32 s6, s6, 0
	s_add_i32 s8, s6, 0x16800
	s_lshl_b64 s[6:7], s[52:53], 1
	s_waitcnt lgkmcnt(0)
	s_add_u32 s4, s4, s6
	s_addc_u32 s5, s5, s7
	s_lshl_b32 s6, s96, 1
	v_lshlrev_b32_e32 v2, 2, v36
	s_add_u32 s4, s4, s6
	v_and_b32_e32 v2, 60, v2
	v_bfe_u32 v58, v36, 4, 4
	s_addc_u32 s5, s5, 0
	s_lshl_b32 s6, s48, 1
	v_lshlrev_b32_e32 v37, 2, v2
	v_lshlrev_b32_e32 v40, 8, v58
	s_add_u32 s4, s4, s6
	v_add3_u32 v37, s8, v37, v40
	s_addc_u32 s5, s5, 0
	v_lshlrev_b32_e32 v2, 1, v2
	ds_read_b128 v[40:43], v37
	ds_read_b128 v[44:47], v37 offset:8192
	v_lshl_add_u64 v[48:49], s[4:5], 0, v[2:3]
	v_lshl_add_u64 v[56:57], v[48:49], 0, s[50:51]
	ds_read_b128 v[48:51], v37 offset:4096
	ds_read_b128 v[52:55], v37 offset:12288
	v_lshl_add_u32 v37, v58, 11, s97
	s_waitcnt lgkmcnt(2)
	v_pk_add_f32 v[42:43], v[42:43], v[46:47]
	v_pk_add_f32 v[40:41], v[40:41], v[44:45]
	v_add_u32_e32 v2, 0x20000, v37
	v_cvt_pk_bf16_f32 v40, v40, v41
	v_cvt_pk_bf16_f32 v41, v42, v43
	v_lshl_add_u64 v[42:43], v[2:3], 1, v[56:57]
	s_andn2_b32 s4, 1, s39
	global_store_dwordx2 v[42:43], v[40:41], off
	s_waitcnt lgkmcnt(0)
	v_pk_add_f32 v[40:41], v[50:51], v[54:55]
	s_mul_i32 s4, s4, 0xb400
	v_cvt_pk_bf16_f32 v47, v40, v41
	s_add_i32 s8, s4, 0
	v_lshlrev_b32_e32 v40, 3, v38
	v_pk_add_f32 v[42:43], v[48:49], v[52:53]
	v_add_u32_e32 v41, s8, v40
	v_cvt_pk_bf16_f32 v46, v42, v43
	ds_read2st64_b64 v[42:45], v41 offset0:82 offset1:83
	v_add_u32_e32 v2, 0x28000, v37
	v_lshl_add_u64 v[48:49], v[2:3], 1, v[56:57]
	global_store_dwordx2 v[48:49], v[46:47], off
	ds_read2st64_b64 v[46:49], v41 offset0:84 offset1:85
	s_waitcnt lgkmcnt(1)
	v_add_f32_e32 v2, 0, v42
	v_cmp_lt_u32_sdwa s[4:5], v36, v120 src0_sel:BYTE_0 src1_sel:DWORD
	v_add_f32_e32 v37, 0, v43
	v_cmp_gt_u32_sdwa vcc, v36, s88 src0_sel:BYTE_0 src1_sel:DWORD
	v_cndmask_b32_e64 v43, v2, 0, s[4:5]
	v_cndmask_b32_e64 v42, v37, 0, s[4:5]
	v_add_f32_e32 v50, v44, v43
	v_bfe_u32 v39, v36, 6, 2
	v_add_f32_e32 v51, v45, v42
	v_cndmask_b32_e32 v43, v43, v50, vcc
	v_cndmask_b32_e32 v36, v42, v51, vcc
	v_add_f32_e32 v42, v2, v44
	s_waitcnt lgkmcnt(0)
	v_add_f32_e32 v2, v46, v43
	v_cmp_eq_u32_e32 vcc, 3, v39
	v_add_f32_e32 v37, v37, v45
	v_add_f32_e32 v44, v47, v36
	v_cndmask_b32_e32 v43, v43, v2, vcc
	v_add_f32_e32 v2, v42, v46
	v_add_f32_e32 v2, v2, v48
	v_cndmask_b32_e32 v45, v36, v44, vcc
	v_add_f32_e32 v36, v37, v47
	v_sub_f32_e32 v2, v2, v42
	v_sub_f32_e32 v43, v43, v42
	v_add_f32_e32 v44, v36, v49
	v_mul_f32_e32 v2, 0x3fb8aa3b, v2
	v_mul_f32_e32 v43, 0x3fb8aa3b, v43
	v_exp_f32_e32 v36, v2
	v_sub_f32_e32 v2, v44, v37
	v_exp_f32_e32 v44, v43
	v_sub_f32_e32 v43, v45, v37
	v_mul_f32_e32 v43, 0x3fb8aa3b, v43
	v_exp_f32_e32 v45, v43
	s_waitcnt vmcnt(50)
; template <int SET> DI void h_prep8(const unsigned (&CR)[72], LAS unsigned char* buf, int tgp, int k2, int v64) {
;     float base0 = 0.f, base1 = 0.f, bm0 = 0.f, bm1 = 0.f, bl0 = 0.f, bl1 = 0.f;
; #pragma unroll
;     for (int g = 0; g < 4; ++g) { const f32x2_t tt = *(const LAS f32x2_t*)(buf + H_TOT + (g * 128 + 2 * k2) * 4);
;         if (g < tgp) { base0 += tt[0]; base1 += tt[1]; } if (g < 2) { bm0 += tt[0]; bm1 += tt[1]; } bl0 += tt[0]; bl1 += tt[1]; }
;     const float ebm0 = __expf(bm0), ebm1 = __expf(bm1), elm0 = __expf(bl0 - bm0), elm1 = __expf(bl1 - bm1);
;     float e20 = __expf(base0 - bm0), e21 = __expf(base1 - bm1); unsigned kup0[4], kup1[4];
; #pragma unroll
;     for (int jp = 0; jp < 4; ++jp) {
;         float ku0[2], ku1[2];
; #pragma unroll
;         for (int jj = 0; jj < 2; ++jj) {
;             const int j = 2 * jp + jj;
;             const unsigned fw = CR[24 * SET + 8 + j], qw = CR[24 * SET + j];
;             const float f0 = __expf(bflo(fw)), f1 = __expf(bfhi(fw)), q0 = bflo(qw), q1 = bfhi(qw);
;             e20 *= f0; e21 *= f1;
;             const float e30 = __builtin_amdgcn_rcpf(e20), e31 = __builtin_amdgcn_rcpf(e21);
;             const float kk0 = 1.0f - f0, kk1 = 1.0f - f1;
;             const int t = 8 * tgp + j;
;             *(LAS unsigned*)(buf + H_QS + t * 272 + 4 * k2) = pk2(q0 * e20, q1 * e21);
;             *(LAS unsigned*)(buf + H_KS + t * 272 + 4 * k2) = pk2(kk0 * e30, kk1 * e31);
;             ku0[jj] = kk0 * e30 * elm0; ku1[jj] = kk1 * e31 * elm1;
;         }
;         kup0[jp] = pk2(ku0[0], ku0[1]); kup1[jp] = pk2(ku1[0], ku1[1]);
;     }
;     { u32x4 w; w.x = kup0[0]; w.y = kup0[1]; w.z = kup0[2]; w.w = kup0[3]; *(LAS u32x4*)(buf + H_KU + (2 * k2) * 80 + 16 * tgp) = w;
;       w.x = kup1[0]; w.y = kup1[1]; w.z = kup1[2]; w.w = kup1[3]; *(LAS u32x4*)(buf + H_KU + (2 * k2 + 1) * 80 + 16 * tgp) = w; }
;     if (tgp == 0) { *(LAS f32x2_t*)(buf + H_DEC + 8 * k2) = (f32x2_t){ebm0 * elm0, ebm1 * elm1}; *(LAS f32x2_t*)(buf + H_EBM + 8 * k2) = (f32x2_t){ebm0, ebm1}; }
;     { u32x4 w; w.x = (CR[24 * SET + 16] & 0xffffu) | (CR[24 * SET + 17] << 16); w.y = (CR[24 * SET + 18] & 0xffffu) | (CR[24 * SET + 19] << 16);
;       w.z = (CR[24 * SET + 20] & 0xffffu) | (CR[24 * SET + 21] << 16); w.w = (CR[24 * SET + 22] & 0xffffu) | (CR[24 * SET + 23] << 16);
;       *(LAS u32x4*)(buf + H_VT + v64 * 80 + 16 * tgp) = w; }
; }
	v_lshlrev_b32_e32 v43, 16, v121
	v_mul_f32_e32 v43, 0x3fb8aa3b, v43
	v_exp_f32_e32 v46, v43
	v_and_b32_e32 v43, 0xffff0000, v121
	v_mul_f32_e32 v43, 0x3fb8aa3b, v43
	v_exp_f32_e32 v47, v43
	s_nop 0
	v_lshlrev_b32_e32 v48, 16, v142
	v_and_b32_e32 v49, 0xffff0000, v142
	v_lshlrev_b32_e32 v43, 2, v38
	v_pk_mul_f32 v[44:45], v[46:47], v[44:45]
	v_mul_f32_e32 v2, 0x3fb8aa3b, v2
	v_pk_mul_f32 v[48:49], v[44:45], v[48:49]
	v_rcp_f32_e32 v50, v44
	v_cvt_pk_bf16_f32 v54, v48, v49
	v_mul_u32_u24_e32 v48, 0x880, v39
	v_add3_u32 v43, s8, v43, v48
	v_lshlrev_b32_e32 v48, 16, v122
	v_and_b32_e32 v49, 0xffff0000, v122
	v_mul_f32_e32 v48, 0x3fb8aa3b, v48
	v_mul_f32_e32 v49, 0x3fb8aa3b, v49
	v_exp_f32_e32 v48, v48
	v_exp_f32_e32 v49, v49
	v_rcp_f32_e32 v51, v45
	v_exp_f32_e32 v2, v2
	v_pk_add_f32 v[46:47], v[46:47], 1.0 op_sel_hi:[1,0] neg_lo:[1,0] neg_hi:[1,0]
	v_pk_mul_f32 v[52:53], v[48:49], v[44:45]
	v_pk_add_f32 v[48:49], v[48:49], 1.0 op_sel_hi:[1,0] neg_lo:[1,0] neg_hi:[1,0]
	v_rcp_f32_e32 v44, v52
	v_rcp_f32_e32 v45, v53
	v_pk_mul_f32 v[46:47], v[46:47], v[50:51]
	v_lshlrev_b32_e32 v50, 16, v124
	v_cvt_pk_bf16_f32 v55, v46, v47
	v_pk_mul_f32 v[44:45], v[48:49], v[44:45]
	v_and_b32_e32 v51, 0xffff0000, v124
	v_cvt_pk_bf16_f32 v48, v44, v45
	v_add_u32_e32 v58, 0x4400, v43
	v_mov_b32_e32 v49, v44
	v_mov_b32_e32 v44, v47
	v_pk_mul_f32 v[50:51], v[52:53], v[50:51]
	ds_write2_b32 v58, v55, v48 offset1:68
	v_mov_b32_e32 v48, v46
	v_pk_mul_f32 v[46:47], v[2:3], v[44:45] op_sel_hi:[0,1]
	v_lshlrev_b32_e32 v45, 16, v133
	v_cvt_pk_bf16_f32 v50, v50, v51
	v_add_u32_e32 v51, 0x2000, v43
	v_mul_f32_e32 v45, 0x3fb8aa3b, v45
	ds_write2_b32 v51, v54, v50 offset0:128 offset1:196
	v_exp_f32_e32 v50, v45
	v_and_b32_e32 v45, 0xffff0000, v133
	v_mul_f32_e32 v45, 0x3fb8aa3b, v45
	v_exp_f32_e32 v51, v45
	v_pk_mul_f32 v[48:49], v[36:37], v[48:49] op_sel_hi:[0,1]
	v_cvt_pk_bf16_f32 v44, v48, v49
	v_cvt_pk_bf16_f32 v48, v46, v47
	v_lshlrev_b32_e32 v46, 16, v123
	v_and_b32_e32 v47, 0xffff0000, v123
	v_pk_mul_f32 v[52:53], v[50:51], v[52:53]
	v_lshlrev_b32_e32 v49, 16, v144
	v_pk_mul_f32 v[46:47], v[52:53], v[46:47]
	v_mul_f32_e32 v49, 0x3fb8aa3b, v49
	v_cvt_pk_bf16_f32 v45, v46, v47
	v_pk_add_f32 v[46:47], v[50:51], 1.0 op_sel_hi:[1,0] neg_lo:[1,0] neg_hi:[1,0]
	v_exp_f32_e32 v50, v49
	v_and_b32_e32 v49, 0xffff0000, v144
	v_mul_f32_e32 v49, 0x3fb8aa3b, v49
	v_exp_f32_e32 v51, v49
	v_rcp_f32_e32 v54, v52
	v_rcp_f32_e32 v55, v53
	v_add_u32_e32 v59, 0x2400, v43
	v_pk_mul_f32 v[52:53], v[50:51], v[52:53]
	v_pk_add_f32 v[50:51], v[50:51], 1.0 op_sel_hi:[1,0] neg_lo:[1,0] neg_hi:[1,0]
	v_rcp_f32_e32 v56, v52
	v_rcp_f32_e32 v57, v53
	v_pk_mul_f32 v[46:47], v[46:47], v[54:55]
	v_lshlrev_b32_e32 v54, 16, v143
	v_and_b32_e32 v55, 0xffff0000, v143
	v_pk_mul_f32 v[54:55], v[52:53], v[54:55]
	v_pk_mul_f32 v[50:51], v[50:51], v[56:57]
	v_cvt_pk_bf16_f32 v54, v54, v55
	v_cvt_pk_bf16_f32 v49, v46, v47
	ds_write2_b32 v59, v45, v54 offset0:8 offset1:76
	v_cvt_pk_bf16_f32 v45, v50, v51
	ds_write2_b32 v58, v49, v45 offset0:136 offset1:204
	v_lshlrev_b32_e32 v49, 16, v150
	v_mov_b32_e32 v55, v50
	v_mov_b32_e32 v50, v47
	v_mul_f32_e32 v49, 0x3fb8aa3b, v49
	v_mov_b32_e32 v54, v46
	v_pk_mul_f32 v[46:47], v[2:3], v[50:51] op_sel_hi:[0,1]
	v_exp_f32_e32 v50, v49
	v_and_b32_e32 v49, 0xffff0000, v150
	v_mul_f32_e32 v49, 0x3fb8aa3b, v49
	v_exp_f32_e32 v51, v49
	v_cvt_pk_bf16_f32 v49, v46, v47
	v_lshlrev_b32_e32 v46, 16, v145
	v_and_b32_e32 v47, 0xffff0000, v145
	v_pk_mul_f32 v[52:53], v[50:51], v[52:53]
	v_pk_mul_f32 v[54:55], v[36:37], v[54:55] op_sel_hi:[0,1]
	v_pk_mul_f32 v[46:47], v[52:53], v[46:47]
	v_cvt_pk_bf16_f32 v45, v54, v55
	v_cvt_pk_bf16_f32 v58, v46, v47
	v_pk_add_f32 v[46:47], v[50:51], 1.0 op_sel_hi:[1,0] neg_lo:[1,0] neg_hi:[1,0]
	v_lshlrev_b32_e32 v50, 16, v164
	v_and_b32_e32 v51, 0xffff0000, v164
	v_mul_f32_e32 v50, 0x3fb8aa3b, v50
	v_mul_f32_e32 v51, 0x3fb8aa3b, v51
	v_exp_f32_e32 v50, v50
	v_exp_f32_e32 v51, v51
	v_rcp_f32_e32 v54, v52
	v_rcp_f32_e32 v55, v53
	v_add_u32_e32 v62, 0x4800, v43
	v_pk_mul_f32 v[52:53], v[50:51], v[52:53]
	v_pk_add_f32 v[50:51], v[50:51], 1.0 op_sel_hi:[1,0] neg_lo:[1,0] neg_hi:[1,0]
	v_rcp_f32_e32 v56, v52
	v_rcp_f32_e32 v57, v53
	v_pk_mul_f32 v[46:47], v[46:47], v[54:55]
	v_lshlrev_b32_e32 v54, 16, v159
	v_and_b32_e32 v55, 0xffff0000, v159
	v_pk_mul_f32 v[54:55], v[52:53], v[54:55]
	v_pk_mul_f32 v[50:51], v[50:51], v[56:57]
	v_cvt_pk_bf16_f32 v54, v54, v55
	v_cvt_pk_bf16_f32 v60, v46, v47
	ds_write2_b32 v59, v58, v54 offset0:144 offset1:212
	v_cvt_pk_bf16_f32 v54, v50, v51
	ds_write2_b32 v62, v60, v54 offset0:16 offset1:84
	v_mov_b32_e32 v54, v46
	v_mov_b32_e32 v55, v50
	v_mov_b32_e32 v50, v47
	v_lshlrev_b32_e32 v47, 16, v171
	v_pk_mul_f32 v[54:55], v[36:37], v[54:55] op_sel_hi:[0,1]
	v_mul_f32_e32 v47, 0x3fb8aa3b, v47
	v_cvt_pk_bf16_f32 v46, v54, v55
	v_exp_f32_e32 v54, v47
	v_and_b32_e32 v47, 0xffff0000, v171
	v_mul_f32_e32 v47, 0x3fb8aa3b, v47
	v_exp_f32_e32 v55, v47
	v_pk_mul_f32 v[50:51], v[2:3], v[50:51] op_sel_hi:[0,1]
	v_cvt_pk_bf16_f32 v50, v50, v51
	s_nop 0
	v_lshlrev_b32_e32 v56, 16, v184
	v_and_b32_e32 v57, 0xffff0000, v184
	v_pk_mul_f32 v[52:53], v[54:55], v[52:53]
	v_lshlrev_b32_e32 v51, 16, v174
	v_pk_mul_f32 v[56:57], v[52:53], v[56:57]
	v_mul_f32_e32 v51, 0x3fb8aa3b, v51
	v_cvt_pk_bf16_f32 v47, v56, v57
	v_exp_f32_e32 v56, v51
	v_and_b32_e32 v51, 0xffff0000, v174
	v_mul_f32_e32 v51, 0x3fb8aa3b, v51
	v_exp_f32_e32 v57, v51
	v_rcp_f32_e32 v58, v52
	v_rcp_f32_e32 v59, v53
	v_pk_add_f32 v[54:55], v[54:55], 1.0 op_sel_hi:[1,0] neg_lo:[1,0] neg_hi:[1,0]
	v_pk_mul_f32 v[52:53], v[56:57], v[52:53]
	v_add_u32_e32 v43, 0x2800, v43
	v_pk_mul_f32 v[54:55], v[54:55], v[58:59]
	v_lshlrev_b32_e32 v58, 16, v177
	v_and_b32_e32 v59, 0xffff0000, v177
	v_rcp_f32_e32 v60, v52
	v_rcp_f32_e32 v61, v53
	v_pk_mul_f32 v[52:53], v[52:53], v[58:59]
	v_cvt_pk_bf16_f32 v51, v54, v55
	v_cvt_pk_bf16_f32 v52, v52, v53
	ds_write2_b32 v43, v47, v52 offset0:24 offset1:92
	v_pk_add_f32 v[52:53], v[56:57], 1.0 op_sel_hi:[1,0] neg_lo:[1,0] neg_hi:[1,0]
	v_mov_b32_e32 v56, v54
	v_pk_mul_f32 v[52:53], v[52:53], v[60:61]
	s_nop 0
	v_cvt_pk_bf16_f32 v43, v52, v53
	v_mov_b32_e32 v57, v52
	v_mov_b32_e32 v52, v55
	v_pk_mul_f32 v[52:53], v[2:3], v[52:53] op_sel_hi:[0,1]
	ds_write2_b32 v62, v51, v43 offset0:152 offset1:220
	v_pk_mul_f32 v[56:57], v[36:37], v[56:57] op_sel_hi:[0,1]
	v_cvt_pk_bf16_f32 v51, v52, v53
	v_mul_u32_u24_e32 v52, 0xa0, v38
	v_lshlrev_b32_e32 v43, 4, v39
	v_cvt_pk_bf16_f32 v47, v56, v57
	v_add3_u32 v52, s8, v52, v43
	ds_write_b128 v52, v[44:47] offset:26112
	ds_write_b128 v52, v[48:51] offset:26192
	s_and_saveexec_b64 s[6:7], s[4:5]
	s_cbranch_execz .LBB0_436
	v_mul_f32_e32 v42, 0x3fb8aa3b, v42
	v_mul_f32_e32 v37, 0x3fb8aa3b, v37
	v_exp_f32_e32 v44, v42
	v_exp_f32_e32 v45, v37
	v_mov_b32_e32 v37, v2
	v_pk_mul_f32 v[36:37], v[44:45], v[36:37]
	ds_write2st64_b64 v41, v[36:37], v[44:45] offset0:81 offset1:86
; #define LAS __attribute__((address_space(3)))
; template <int SET> DI void h_totals8(const unsigned (&CR)[72], LAS unsigned char* buf, int tgp, int k2) {
;     float lo = 0.f, hi = 0.f;
; #pragma unroll
;     for (int j = 0; j < 8; ++j) { lo += bflo(CR[24 * SET + 8 + j]); hi += bfhi(CR[24 * SET + 8 + j]); }
;     *(LAS f32x2_t*)(buf + H_TOT + (tgp * 128 + 2 * k2) * 4) = (f32x2_t){lo, hi};
; }
; template <int SET> DI void h_prep8(const unsigned (&CR)[72], LAS unsigned char* buf, int tgp, int k2, int v64) {
;     ...
;     { u32x4 w; w.x = (CR[24 * SET + 16] & 0xffffu) | (CR[24 * SET + 17] << 16); w.y = (CR[24 * SET + 18] & 0xffffu) | (CR[24 * SET + 19] << 16);
;       w.z = (CR[24 * SET + 20] & 0xffffu) | (CR[24 * SET + 21] << 16); w.w = (CR[24 * SET + 22] & 0xffffu) | (CR[24 * SET + 23] << 16);
;       *(LAS u32x4*)(buf + H_VT + v64 * 80 + 16 * tgp) = w; }
.LBB0_436:
	s_or_b64 exec, exec, s[6:7]
	v_mul_u32_u24_e32 v2, 0x50, v38
	v_lshl_add_u32 v44, v185, 16, v189
	v_lshl_add_u32 v45, v186, 16, v188
	v_lshl_add_u32 v46, v192, 16, v191
	v_lshl_add_u32 v47, v187, 16, v190
	v_add3_u32 v2, s8, v2, v43
	s_cmp_gt_u32 s39, 59
	ds_write_b128 v2, v[44:47] offset:36352
	s_cbranch_scc1 .LBB0_439
	s_nop 0
	s_waitcnt vmcnt(26)
	v_lshlrev_b32_e32 v36, 16, v130
	v_and_b32_e32 v37, 0xffff0000, v130
	s_nop 0
	v_lshlrev_b32_e32 v42, 16, v132
	v_and_b32_e32 v43, 0xffff0000, v132
	v_pk_add_f32 v[36:37], v[36:37], 0 op_sel_hi:[1,0]
	s_nop 0
	v_lshlrev_b32_e32 v44, 16, v141
	v_and_b32_e32 v45, 0xffff0000, v141
	v_pk_add_f32 v[36:37], v[36:37], v[42:43]
	s_nop 0
	v_lshlrev_b32_e32 v46, 16, v158
	v_and_b32_e32 v47, 0xffff0000, v158
	v_pk_add_f32 v[36:37], v[36:37], v[44:45]
	v_lshlrev_b32_e32 v48, 16, v156
	v_and_b32_e32 v49, 0xffff0000, v156
	v_pk_add_f32 v[36:37], v[36:37], v[46:47]
	s_bitcmp1_b32 s39, 0
	v_lshlrev_b32_e32 v50, 16, v168
	v_and_b32_e32 v51, 0xffff0000, v168
	v_pk_add_f32 v[36:37], v[36:37], v[48:49]
	s_cselect_b32 s4, 0xb400, 0
	s_nop 0
	v_lshlrev_b32_e32 v52, 16, v173
	v_and_b32_e32 v53, 0xffff0000, v173
	v_pk_add_f32 v[36:37], v[36:37], v[50:51]
	s_add_i32 s4, s4, 0
	s_nop 0
	v_lshlrev_b32_e32 v54, 16, v176
	v_and_b32_e32 v55, 0xffff0000, v176
	v_pk_add_f32 v[36:37], v[36:37], v[52:53]
	v_lshlrev_b32_e32 v2, 9, v39
	v_pk_add_f32 v[36:37], v[36:37], v[54:55]
	v_add3_u32 v2, s4, v2, v40
	ds_write_b64 v2, v[36:37] offset:41984
	s_branch .LBB0_439
